# nt11 plus: P9b row blocks - readlane of the hid value hoisted above the fp8 converts, 80 s_nop 1 removed
# speedup vs baseline: 1.0050x; 1.0050x over previous
.LBB0_1104:
	s_cmp_lt_i32 s16, 2
	s_cbranch_scc1 .LBB0_1293
	s_waitcnt vmcnt(22)
	s_waitcnt lgkmcnt(0)
	v_readlane_b32 s14, v192, 1
	v_cvt_pk_f32_fp8_e32 v[194:195], v36
	v_cvt_pk_f32_fp8_sdwa v[196:197], v36 src0_sel:WORD_1
	v_cvt_pk_f32_fp8_e32 v[198:199], v37
	v_cvt_pk_f32_fp8_sdwa v[200:201], v37 src0_sel:WORD_1
	v_pk_fma_f32 v[188:189], v[194:195], s[14:15], v[188:189] op_sel_hi:[1,0,1]
	v_pk_fma_f32 v[184:185], v[196:197], s[14:15], v[184:185] op_sel_hi:[1,0,1]
	v_pk_fma_f32 v[180:181], s[14:15], v[198:199], v[180:181] op_sel_hi:[0,1,1]
	v_pk_fma_f32 v[176:177], s[14:15], v[200:201], v[176:177] op_sel_hi:[0,1,1]
	v_cvt_pk_f32_fp8_e32 v[194:195], v38
	v_cvt_pk_f32_fp8_sdwa v[196:197], v38 src0_sel:WORD_1
	v_cvt_pk_f32_fp8_e32 v[198:199], v39
	v_cvt_pk_f32_fp8_sdwa v[200:201], v39 src0_sel:WORD_1
	v_pk_fma_f32 v[190:191], s[14:15], v[194:195], v[190:191] op_sel_hi:[0,1,1]
	v_pk_fma_f32 v[186:187], s[14:15], v[196:197], v[186:187] op_sel_hi:[0,1,1]
	v_pk_fma_f32 v[182:183], s[14:15], v[198:199], v[182:183] op_sel_hi:[0,1,1]
	v_pk_fma_f32 v[178:179], s[14:15], v[200:201], v[178:179] op_sel_hi:[0,1,1]
	s_cmp_lt_i32 s16, 3
	s_cbranch_scc0 .LBB0_1294

.LBB0_1107:
	s_waitcnt vmcnt(11)
	s_waitcnt lgkmcnt(0)
	v_readlane_b32 s14, v192, 3
	v_cvt_pk_f32_fp8_e32 v[194:195], v20
	v_cvt_pk_f32_fp8_sdwa v[196:197], v20 src0_sel:WORD_1
	v_cvt_pk_f32_fp8_e32 v[198:199], v21
	v_cvt_pk_f32_fp8_sdwa v[200:201], v21 src0_sel:WORD_1
	v_pk_fma_f32 v[188:189], v[194:195], s[14:15], v[188:189] op_sel_hi:[1,0,1]
	v_pk_fma_f32 v[184:185], v[196:197], s[14:15], v[184:185] op_sel_hi:[1,0,1]
	v_pk_fma_f32 v[180:181], s[14:15], v[198:199], v[180:181] op_sel_hi:[0,1,1]
	v_pk_fma_f32 v[176:177], s[14:15], v[200:201], v[176:177] op_sel_hi:[0,1,1]
	v_cvt_pk_f32_fp8_e32 v[194:195], v22
	v_cvt_pk_f32_fp8_sdwa v[196:197], v22 src0_sel:WORD_1
	v_cvt_pk_f32_fp8_e32 v[198:199], v23
	v_cvt_pk_f32_fp8_sdwa v[200:201], v23 src0_sel:WORD_1
	v_pk_fma_f32 v[190:191], s[14:15], v[194:195], v[190:191] op_sel_hi:[0,1,1]
	v_pk_fma_f32 v[186:187], s[14:15], v[196:197], v[186:187] op_sel_hi:[0,1,1]
	v_pk_fma_f32 v[182:183], s[14:15], v[198:199], v[182:183] op_sel_hi:[0,1,1]
	v_pk_fma_f32 v[178:179], s[14:15], v[200:201], v[178:179] op_sel_hi:[0,1,1]
	s_cmp_lt_i32 s16, 5
	s_cbranch_scc0 .LBB0_1296

.LBB0_1109:
	s_waitcnt vmcnt(18)
	s_waitcnt lgkmcnt(0)
	v_readlane_b32 s14, v192, 5
	v_cvt_pk_f32_fp8_e32 v[194:195], v8
	v_cvt_pk_f32_fp8_sdwa v[196:197], v8 src0_sel:WORD_1
	v_cvt_pk_f32_fp8_e32 v[198:199], v9
	v_cvt_pk_f32_fp8_sdwa v[200:201], v9 src0_sel:WORD_1
	v_pk_fma_f32 v[188:189], v[194:195], s[14:15], v[188:189] op_sel_hi:[1,0,1]
	v_pk_fma_f32 v[184:185], v[196:197], s[14:15], v[184:185] op_sel_hi:[1,0,1]
	v_pk_fma_f32 v[180:181], s[14:15], v[198:199], v[180:181] op_sel_hi:[0,1,1]
	v_pk_fma_f32 v[176:177], s[14:15], v[200:201], v[176:177] op_sel_hi:[0,1,1]
	v_cvt_pk_f32_fp8_e32 v[194:195], v10
	v_cvt_pk_f32_fp8_sdwa v[196:197], v10 src0_sel:WORD_1
	v_cvt_pk_f32_fp8_e32 v[198:199], v11
	v_cvt_pk_f32_fp8_sdwa v[200:201], v11 src0_sel:WORD_1
	v_pk_fma_f32 v[190:191], s[14:15], v[194:195], v[190:191] op_sel_hi:[0,1,1]
	v_pk_fma_f32 v[186:187], s[14:15], v[196:197], v[186:187] op_sel_hi:[0,1,1]
	v_pk_fma_f32 v[182:183], s[14:15], v[198:199], v[182:183] op_sel_hi:[0,1,1]
	v_pk_fma_f32 v[178:179], s[14:15], v[200:201], v[178:179] op_sel_hi:[0,1,1]
	s_cmp_lt_i32 s16, 7
	s_cbranch_scc0 .LBB0_1298

.LBB0_1113:
	s_and_b64 vcc, exec, s[14:15]
	v_mov_b64_e32 v[200:201], v[144:145]
	v_mov_b64_e32 v[204:205], v[146:147]
	v_mov_b64_e32 v[206:207], v[148:149]
	v_mov_b64_e32 v[208:209], v[150:151]
	s_waitcnt lgkmcnt(0)
	v_mov_b64_e32 v[192:193], v[152:153]
	v_mov_b64_e32 v[194:195], v[154:155]
	v_mov_b64_e32 v[196:197], v[156:157]
	v_mov_b64_e32 v[198:199], v[158:159]
	s_cbranch_vccz .LBB0_1125
	v_lshl_add_u32 v176, v234, 2, s17
	ds_read_b32 v176, v176 offset:5120
	s_cmp_lt_i32 s16, 1
	v_mov_b64_e32 v[198:199], v[158:159]
	v_mov_b64_e32 v[196:197], v[156:157]
	v_mov_b64_e32 v[194:195], v[154:155]
	v_mov_b64_e32 v[192:193], v[152:153]
	v_mov_b64_e32 v[208:209], v[150:151]
	v_mov_b64_e32 v[206:207], v[148:149]
	v_mov_b64_e32 v[204:205], v[146:147]
	v_mov_b64_e32 v[200:201], v[144:145]
	s_cbranch_scc1 .LBB0_1116
	s_waitcnt vmcnt(23)
	s_waitcnt lgkmcnt(0)
	v_readlane_b32 s14, v176, 0
	v_cvt_pk_f32_fp8_e32 v[178:179], v48
	v_cvt_pk_f32_fp8_sdwa v[180:181], v48 src0_sel:WORD_1
	v_cvt_pk_f32_fp8_e32 v[182:183], v49
	v_cvt_pk_f32_fp8_sdwa v[184:185], v49 src0_sel:WORD_1
	v_pk_fma_f32 v[198:199], v[178:179], s[14:15], v[158:159] op_sel_hi:[1,0,1]
	v_pk_fma_f32 v[196:197], v[180:181], s[14:15], v[156:157] op_sel_hi:[1,0,1]
	v_pk_fma_f32 v[194:195], s[14:15], v[182:183], v[154:155] op_sel_hi:[0,1,1]
	v_pk_fma_f32 v[192:193], s[14:15], v[184:185], v[152:153] op_sel_hi:[0,1,1]
	s_waitcnt vmcnt(9)
	v_cvt_pk_f32_fp8_e32 v[178:179], v50
	v_cvt_pk_f32_fp8_sdwa v[180:181], v50 src0_sel:WORD_1
	v_cvt_pk_f32_fp8_e32 v[182:183], v51
	v_cvt_pk_f32_fp8_sdwa v[184:185], v51 src0_sel:WORD_1
	v_pk_fma_f32 v[208:209], s[14:15], v[178:179], v[150:151] op_sel_hi:[0,1,1]
	v_pk_fma_f32 v[206:207], s[14:15], v[180:181], v[148:149] op_sel_hi:[0,1,1]
	v_pk_fma_f32 v[204:205], s[14:15], v[182:183], v[146:147] op_sel_hi:[0,1,1]
	v_pk_fma_f32 v[200:201], s[14:15], v[184:185], v[144:145] op_sel_hi:[0,1,1]
.LBB0_1116:
	s_cmp_lt_i32 s16, 2
	s_cbranch_scc1 .LBB0_1299
	s_waitcnt vmcnt(22)
	s_waitcnt lgkmcnt(0)
	v_readlane_b32 s14, v176, 1
	v_cvt_pk_f32_fp8_e32 v[178:179], v36
	v_cvt_pk_f32_fp8_sdwa v[180:181], v36 src0_sel:WORD_1
	v_cvt_pk_f32_fp8_e32 v[182:183], v37
	v_cvt_pk_f32_fp8_sdwa v[184:185], v37 src0_sel:WORD_1
	v_pk_fma_f32 v[198:199], v[178:179], s[14:15], v[198:199] op_sel_hi:[1,0,1]
	v_pk_fma_f32 v[196:197], v[180:181], s[14:15], v[196:197] op_sel_hi:[1,0,1]
	v_pk_fma_f32 v[194:195], s[14:15], v[182:183], v[194:195] op_sel_hi:[0,1,1]
	v_pk_fma_f32 v[192:193], s[14:15], v[184:185], v[192:193] op_sel_hi:[0,1,1]
	v_cvt_pk_f32_fp8_e32 v[178:179], v38
	v_cvt_pk_f32_fp8_sdwa v[180:181], v38 src0_sel:WORD_1
	v_cvt_pk_f32_fp8_e32 v[182:183], v39
	v_cvt_pk_f32_fp8_sdwa v[184:185], v39 src0_sel:WORD_1
	v_pk_fma_f32 v[208:209], s[14:15], v[178:179], v[208:209] op_sel_hi:[0,1,1]
	v_pk_fma_f32 v[206:207], s[14:15], v[180:181], v[206:207] op_sel_hi:[0,1,1]
	v_pk_fma_f32 v[204:205], s[14:15], v[182:183], v[204:205] op_sel_hi:[0,1,1]
	v_pk_fma_f32 v[200:201], s[14:15], v[184:185], v[200:201] op_sel_hi:[0,1,1]
	s_cmp_lt_i32 s16, 3
	s_cbranch_scc0 .LBB0_1300

.LBB0_1119:
	s_waitcnt vmcnt(11)
	s_waitcnt lgkmcnt(0)
	v_readlane_b32 s14, v176, 3
	v_cvt_pk_f32_fp8_e32 v[178:179], v20
	v_cvt_pk_f32_fp8_sdwa v[180:181], v20 src0_sel:WORD_1
	v_cvt_pk_f32_fp8_e32 v[182:183], v21
	v_cvt_pk_f32_fp8_sdwa v[184:185], v21 src0_sel:WORD_1
	v_pk_fma_f32 v[198:199], v[178:179], s[14:15], v[198:199] op_sel_hi:[1,0,1]
	v_pk_fma_f32 v[196:197], v[180:181], s[14:15], v[196:197] op_sel_hi:[1,0,1]
	v_pk_fma_f32 v[194:195], s[14:15], v[182:183], v[194:195] op_sel_hi:[0,1,1]
	v_pk_fma_f32 v[192:193], s[14:15], v[184:185], v[192:193] op_sel_hi:[0,1,1]
	v_cvt_pk_f32_fp8_e32 v[178:179], v22
	v_cvt_pk_f32_fp8_sdwa v[180:181], v22 src0_sel:WORD_1
	v_cvt_pk_f32_fp8_e32 v[182:183], v23
	v_cvt_pk_f32_fp8_sdwa v[184:185], v23 src0_sel:WORD_1
	v_pk_fma_f32 v[208:209], s[14:15], v[178:179], v[208:209] op_sel_hi:[0,1,1]
	v_pk_fma_f32 v[206:207], s[14:15], v[180:181], v[206:207] op_sel_hi:[0,1,1]
	v_pk_fma_f32 v[204:205], s[14:15], v[182:183], v[204:205] op_sel_hi:[0,1,1]
	v_pk_fma_f32 v[200:201], s[14:15], v[184:185], v[200:201] op_sel_hi:[0,1,1]
	s_cmp_lt_i32 s16, 5
	s_cbranch_scc0 .LBB0_1302

.LBB0_1121:
	s_waitcnt vmcnt(18)
	s_waitcnt lgkmcnt(0)
	v_readlane_b32 s14, v176, 5
	v_cvt_pk_f32_fp8_e32 v[178:179], v8
	v_cvt_pk_f32_fp8_sdwa v[180:181], v8 src0_sel:WORD_1
	v_cvt_pk_f32_fp8_e32 v[182:183], v9
	v_cvt_pk_f32_fp8_sdwa v[184:185], v9 src0_sel:WORD_1
	v_pk_fma_f32 v[198:199], v[178:179], s[14:15], v[198:199] op_sel_hi:[1,0,1]
	v_pk_fma_f32 v[196:197], v[180:181], s[14:15], v[196:197] op_sel_hi:[1,0,1]
	v_pk_fma_f32 v[194:195], s[14:15], v[182:183], v[194:195] op_sel_hi:[0,1,1]
	v_pk_fma_f32 v[192:193], s[14:15], v[184:185], v[192:193] op_sel_hi:[0,1,1]
	v_cvt_pk_f32_fp8_e32 v[178:179], v10
	v_cvt_pk_f32_fp8_sdwa v[180:181], v10 src0_sel:WORD_1
	v_cvt_pk_f32_fp8_e32 v[182:183], v11
	v_cvt_pk_f32_fp8_sdwa v[184:185], v11 src0_sel:WORD_1
	v_pk_fma_f32 v[208:209], s[14:15], v[178:179], v[208:209] op_sel_hi:[0,1,1]
	v_pk_fma_f32 v[206:207], s[14:15], v[180:181], v[206:207] op_sel_hi:[0,1,1]
	v_pk_fma_f32 v[204:205], s[14:15], v[182:183], v[204:205] op_sel_hi:[0,1,1]
	v_pk_fma_f32 v[200:201], s[14:15], v[184:185], v[200:201] op_sel_hi:[0,1,1]
	s_cmp_lt_i32 s16, 7
	s_cbranch_scc0 .LBB0_1304

.LBB0_1126:
	s_andn2_b64 vcc, exec, s[14:15]
	v_mov_b64_e32 v[224:225], v[160:161]
	v_mov_b64_e32 v[222:223], v[162:163]
	v_mov_b64_e32 v[220:221], v[164:165]
	v_mov_b64_e32 v[218:219], v[166:167]
	v_mov_b64_e32 v[216:217], v[168:169]
	v_mov_b64_e32 v[214:215], v[170:171]
	v_mov_b64_e32 v[212:213], v[172:173]
	v_mov_b64_e32 v[210:211], v[174:175]
	s_cbranch_vccnz .LBB0_1138
	v_lshl_add_u32 v176, v234, 2, s17
	ds_read_b32 v176, v176 offset:4608
	s_cmp_lt_i32 s16, 1
	v_mov_b64_e32 v[210:211], v[174:175]
	v_mov_b64_e32 v[212:213], v[172:173]
	v_mov_b64_e32 v[214:215], v[170:171]
	v_mov_b64_e32 v[216:217], v[168:169]
	v_mov_b64_e32 v[218:219], v[166:167]
	v_mov_b64_e32 v[220:221], v[164:165]
	v_mov_b64_e32 v[222:223], v[162:163]
	v_mov_b64_e32 v[224:225], v[160:161]
	s_cbranch_scc1 .LBB0_1129
	s_waitcnt vmcnt(23)
	s_waitcnt lgkmcnt(0)
	v_readlane_b32 s14, v176, 0
	v_cvt_pk_f32_fp8_e32 v[178:179], v48
	v_cvt_pk_f32_fp8_sdwa v[180:181], v48 src0_sel:WORD_1
	v_cvt_pk_f32_fp8_e32 v[182:183], v49
	v_cvt_pk_f32_fp8_sdwa v[184:185], v49 src0_sel:WORD_1
	v_pk_fma_f32 v[210:211], v[178:179], s[14:15], v[174:175] op_sel_hi:[1,0,1]
	v_pk_fma_f32 v[212:213], v[180:181], s[14:15], v[172:173] op_sel_hi:[1,0,1]
	v_pk_fma_f32 v[214:215], s[14:15], v[182:183], v[170:171] op_sel_hi:[0,1,1]
	v_pk_fma_f32 v[216:217], s[14:15], v[184:185], v[168:169] op_sel_hi:[0,1,1]
	s_waitcnt vmcnt(9)
	v_cvt_pk_f32_fp8_e32 v[178:179], v50
	v_cvt_pk_f32_fp8_sdwa v[180:181], v50 src0_sel:WORD_1
	v_cvt_pk_f32_fp8_e32 v[182:183], v51
	v_cvt_pk_f32_fp8_sdwa v[184:185], v51 src0_sel:WORD_1
	v_pk_fma_f32 v[218:219], s[14:15], v[178:179], v[166:167] op_sel_hi:[0,1,1]
	v_pk_fma_f32 v[220:221], s[14:15], v[180:181], v[164:165] op_sel_hi:[0,1,1]
	v_pk_fma_f32 v[222:223], s[14:15], v[182:183], v[162:163] op_sel_hi:[0,1,1]
	v_pk_fma_f32 v[224:225], s[14:15], v[184:185], v[160:161] op_sel_hi:[0,1,1]
.LBB0_1129:
	s_cmp_lt_i32 s16, 2
	s_cbranch_scc1 .LBB0_1275
	s_waitcnt vmcnt(22)
	s_waitcnt lgkmcnt(0)
	v_readlane_b32 s14, v176, 1
	v_cvt_pk_f32_fp8_e32 v[178:179], v36
	v_cvt_pk_f32_fp8_sdwa v[180:181], v36 src0_sel:WORD_1
	v_cvt_pk_f32_fp8_e32 v[182:183], v37
	v_cvt_pk_f32_fp8_sdwa v[184:185], v37 src0_sel:WORD_1
	v_pk_fma_f32 v[210:211], v[178:179], s[14:15], v[210:211] op_sel_hi:[1,0,1]
	v_pk_fma_f32 v[212:213], v[180:181], s[14:15], v[212:213] op_sel_hi:[1,0,1]
	v_pk_fma_f32 v[214:215], s[14:15], v[182:183], v[214:215] op_sel_hi:[0,1,1]
	v_pk_fma_f32 v[216:217], s[14:15], v[184:185], v[216:217] op_sel_hi:[0,1,1]
	v_cvt_pk_f32_fp8_e32 v[178:179], v38
	v_cvt_pk_f32_fp8_sdwa v[180:181], v38 src0_sel:WORD_1
	v_cvt_pk_f32_fp8_e32 v[182:183], v39
	v_cvt_pk_f32_fp8_sdwa v[184:185], v39 src0_sel:WORD_1
	v_pk_fma_f32 v[218:219], s[14:15], v[178:179], v[218:219] op_sel_hi:[0,1,1]
	v_pk_fma_f32 v[220:221], s[14:15], v[180:181], v[220:221] op_sel_hi:[0,1,1]
	v_pk_fma_f32 v[222:223], s[14:15], v[182:183], v[222:223] op_sel_hi:[0,1,1]
	v_pk_fma_f32 v[224:225], s[14:15], v[184:185], v[224:225] op_sel_hi:[0,1,1]
	s_cmp_lt_i32 s16, 3
	s_cbranch_scc0 .LBB0_1276

.LBB0_1132:
	s_waitcnt vmcnt(11)
	s_waitcnt lgkmcnt(0)
	v_readlane_b32 s14, v176, 3
	v_cvt_pk_f32_fp8_e32 v[178:179], v20
	v_cvt_pk_f32_fp8_sdwa v[180:181], v20 src0_sel:WORD_1
	v_cvt_pk_f32_fp8_e32 v[182:183], v21
	v_cvt_pk_f32_fp8_sdwa v[184:185], v21 src0_sel:WORD_1
	v_pk_fma_f32 v[210:211], v[178:179], s[14:15], v[210:211] op_sel_hi:[1,0,1]
	v_pk_fma_f32 v[212:213], v[180:181], s[14:15], v[212:213] op_sel_hi:[1,0,1]
	v_pk_fma_f32 v[214:215], s[14:15], v[182:183], v[214:215] op_sel_hi:[0,1,1]
	v_pk_fma_f32 v[216:217], s[14:15], v[184:185], v[216:217] op_sel_hi:[0,1,1]
	v_cvt_pk_f32_fp8_e32 v[178:179], v22
	v_cvt_pk_f32_fp8_sdwa v[180:181], v22 src0_sel:WORD_1
	v_cvt_pk_f32_fp8_e32 v[182:183], v23
	v_cvt_pk_f32_fp8_sdwa v[184:185], v23 src0_sel:WORD_1
	v_pk_fma_f32 v[218:219], s[14:15], v[178:179], v[218:219] op_sel_hi:[0,1,1]
	v_pk_fma_f32 v[220:221], s[14:15], v[180:181], v[220:221] op_sel_hi:[0,1,1]
	v_pk_fma_f32 v[222:223], s[14:15], v[182:183], v[222:223] op_sel_hi:[0,1,1]
	v_pk_fma_f32 v[224:225], s[14:15], v[184:185], v[224:225] op_sel_hi:[0,1,1]
	s_cmp_lt_i32 s16, 5
	s_cbranch_scc0 .LBB0_1278

.LBB0_1134:
	s_waitcnt vmcnt(18)
	s_waitcnt lgkmcnt(0)
	v_readlane_b32 s14, v176, 5
	v_cvt_pk_f32_fp8_e32 v[178:179], v8
	v_cvt_pk_f32_fp8_sdwa v[180:181], v8 src0_sel:WORD_1
	v_cvt_pk_f32_fp8_e32 v[182:183], v9
	v_cvt_pk_f32_fp8_sdwa v[184:185], v9 src0_sel:WORD_1
	v_pk_fma_f32 v[210:211], v[178:179], s[14:15], v[210:211] op_sel_hi:[1,0,1]
	v_pk_fma_f32 v[212:213], v[180:181], s[14:15], v[212:213] op_sel_hi:[1,0,1]
	v_pk_fma_f32 v[214:215], s[14:15], v[182:183], v[214:215] op_sel_hi:[0,1,1]
	v_pk_fma_f32 v[216:217], s[14:15], v[184:185], v[216:217] op_sel_hi:[0,1,1]
	v_cvt_pk_f32_fp8_e32 v[178:179], v10
	v_cvt_pk_f32_fp8_sdwa v[180:181], v10 src0_sel:WORD_1
	v_cvt_pk_f32_fp8_e32 v[182:183], v11
	v_cvt_pk_f32_fp8_sdwa v[184:185], v11 src0_sel:WORD_1
	v_pk_fma_f32 v[218:219], s[14:15], v[178:179], v[218:219] op_sel_hi:[0,1,1]
	v_pk_fma_f32 v[220:221], s[14:15], v[180:181], v[220:221] op_sel_hi:[0,1,1]
	v_pk_fma_f32 v[222:223], s[14:15], v[182:183], v[222:223] op_sel_hi:[0,1,1]
	v_pk_fma_f32 v[224:225], s[14:15], v[184:185], v[224:225] op_sel_hi:[0,1,1]
	s_cmp_lt_i32 s16, 7
	s_cbranch_scc0 .LBB0_1280

.LBB0_1139:
	s_andn2_b64 vcc, exec, s[14:15]
	s_cbranch_vccnz .LBB0_1149
	v_lshl_add_u32 v176, v234, 2, s17
	ds_read_b32 v176, v176 offset:4096
	s_cmp_lt_i32 s16, 1
	s_cbranch_scc1 .LBB0_1142
	s_waitcnt vmcnt(23)
	s_waitcnt lgkmcnt(0)
	v_readlane_b32 s14, v176, 0
	v_cvt_pk_f32_fp8_e32 v[178:179], v48
	v_cvt_pk_f32_fp8_sdwa v[180:181], v48 src0_sel:WORD_1
	v_cvt_pk_f32_fp8_e32 v[182:183], v49
	v_cvt_pk_f32_fp8_sdwa v[48:49], v49 src0_sel:WORD_1
	v_pk_fma_f32 v[126:127], v[178:179], s[14:15], v[126:127] op_sel_hi:[1,0,1]
	v_pk_fma_f32 v[124:125], v[180:181], s[14:15], v[124:125] op_sel_hi:[1,0,1]
	v_pk_fma_f32 v[120:121], s[14:15], v[48:49], v[120:121] op_sel_hi:[0,1,1]
	s_waitcnt vmcnt(9)
	v_cvt_pk_f32_fp8_e32 v[48:49], v50
	v_cvt_pk_f32_fp8_sdwa v[178:179], v50 src0_sel:WORD_1
	v_cvt_pk_f32_fp8_e32 v[180:181], v51
	v_cvt_pk_f32_fp8_sdwa v[50:51], v51 src0_sel:WORD_1
	v_pk_fma_f32 v[122:123], s[14:15], v[182:183], v[122:123] op_sel_hi:[0,1,1]
	v_pk_fma_f32 v[118:119], s[14:15], v[48:49], v[118:119] op_sel_hi:[0,1,1]
	v_pk_fma_f32 v[116:117], s[14:15], v[178:179], v[116:117] op_sel_hi:[0,1,1]
	v_pk_fma_f32 v[114:115], s[14:15], v[180:181], v[114:115] op_sel_hi:[0,1,1]
	v_pk_fma_f32 v[112:113], s[14:15], v[50:51], v[112:113] op_sel_hi:[0,1,1]

.LBB0_1145:
	s_waitcnt vmcnt(10)
	s_waitcnt lgkmcnt(0)
	v_readlane_b32 s14, v176, 3
	v_cvt_pk_f32_fp8_e32 v[32:33], v20
	v_cvt_pk_f32_fp8_sdwa v[34:35], v20 src0_sel:WORD_1
	v_cvt_pk_f32_fp8_e32 v[36:37], v21
	v_cvt_pk_f32_fp8_sdwa v[20:21], v21 src0_sel:WORD_1
	v_pk_fma_f32 v[126:127], v[32:33], s[14:15], v[126:127] op_sel_hi:[1,0,1]
	v_pk_fma_f32 v[124:125], v[34:35], s[14:15], v[124:125] op_sel_hi:[1,0,1]
	v_pk_fma_f32 v[120:121], s[14:15], v[20:21], v[120:121] op_sel_hi:[0,1,1]
	v_cvt_pk_f32_fp8_e32 v[20:21], v22
	v_cvt_pk_f32_fp8_sdwa v[32:33], v22 src0_sel:WORD_1
	v_cvt_pk_f32_fp8_e32 v[34:35], v23
	v_cvt_pk_f32_fp8_sdwa v[22:23], v23 src0_sel:WORD_1
	v_pk_fma_f32 v[122:123], s[14:15], v[36:37], v[122:123] op_sel_hi:[0,1,1]
	v_pk_fma_f32 v[118:119], s[14:15], v[20:21], v[118:119] op_sel_hi:[0,1,1]
	v_pk_fma_f32 v[116:117], s[14:15], v[32:33], v[116:117] op_sel_hi:[0,1,1]
	v_pk_fma_f32 v[114:115], s[14:15], v[34:35], v[114:115] op_sel_hi:[0,1,1]
	v_pk_fma_f32 v[112:113], s[14:15], v[22:23], v[112:113] op_sel_hi:[0,1,1]
	s_cmp_lt_i32 s16, 5
	s_cbranch_scc0 .LBB0_1153

.LBB0_1151:
	s_waitcnt vmcnt(10)
	s_waitcnt lgkmcnt(0)
	v_readlane_b32 s14, v176, 2
	v_cvt_pk_f32_fp8_e32 v[36:37], v32
	v_cvt_pk_f32_fp8_sdwa v[38:39], v32 src0_sel:WORD_1
	v_cvt_pk_f32_fp8_e32 v[48:49], v33
	v_cvt_pk_f32_fp8_sdwa v[32:33], v33 src0_sel:WORD_1
	v_pk_fma_f32 v[126:127], v[36:37], s[14:15], v[126:127] op_sel_hi:[1,0,1]
	v_pk_fma_f32 v[124:125], v[38:39], s[14:15], v[124:125] op_sel_hi:[1,0,1]
	v_pk_fma_f32 v[120:121], s[14:15], v[32:33], v[120:121] op_sel_hi:[0,1,1]
	v_cvt_pk_f32_fp8_e32 v[32:33], v34
	v_cvt_pk_f32_fp8_sdwa v[36:37], v34 src0_sel:WORD_1
	v_cvt_pk_f32_fp8_e32 v[38:39], v35
	v_cvt_pk_f32_fp8_sdwa v[34:35], v35 src0_sel:WORD_1
	v_pk_fma_f32 v[122:123], s[14:15], v[48:49], v[122:123] op_sel_hi:[0,1,1]
	v_pk_fma_f32 v[118:119], s[14:15], v[32:33], v[118:119] op_sel_hi:[0,1,1]
	v_pk_fma_f32 v[116:117], s[14:15], v[36:37], v[116:117] op_sel_hi:[0,1,1]
	v_pk_fma_f32 v[114:115], s[14:15], v[38:39], v[114:115] op_sel_hi:[0,1,1]
	v_pk_fma_f32 v[112:113], s[14:15], v[34:35], v[112:113] op_sel_hi:[0,1,1]
	s_cmp_lt_i32 s16, 4
	s_cbranch_scc0 .LBB0_1145

.LBB0_1155:
	s_waitcnt vmcnt(17)
	s_waitcnt lgkmcnt(0)
	v_readlane_b32 s14, v176, 6
	v_cvt_pk_f32_fp8_e32 v[8:9], v4
	v_cvt_pk_f32_fp8_sdwa v[10:11], v4 src0_sel:WORD_1
	v_cvt_pk_f32_fp8_e32 v[16:17], v5
	v_cvt_pk_f32_fp8_sdwa v[4:5], v5 src0_sel:WORD_1
	v_pk_fma_f32 v[126:127], v[8:9], s[14:15], v[126:127] op_sel_hi:[1,0,1]
	v_pk_fma_f32 v[124:125], v[10:11], s[14:15], v[124:125] op_sel_hi:[1,0,1]
	v_pk_fma_f32 v[120:121], s[14:15], v[4:5], v[120:121] op_sel_hi:[0,1,1]
	v_cvt_pk_f32_fp8_e32 v[4:5], v6
	v_cvt_pk_f32_fp8_sdwa v[8:9], v6 src0_sel:WORD_1
	v_cvt_pk_f32_fp8_e32 v[10:11], v7
	v_cvt_pk_f32_fp8_sdwa v[6:7], v7 src0_sel:WORD_1
	v_pk_fma_f32 v[122:123], s[14:15], v[16:17], v[122:123] op_sel_hi:[0,1,1]
	v_pk_fma_f32 v[118:119], s[14:15], v[4:5], v[118:119] op_sel_hi:[0,1,1]
	v_pk_fma_f32 v[116:117], s[14:15], v[8:9], v[116:117] op_sel_hi:[0,1,1]
	v_pk_fma_f32 v[114:115], s[14:15], v[10:11], v[114:115] op_sel_hi:[0,1,1]
	v_pk_fma_f32 v[112:113], s[14:15], v[6:7], v[112:113] op_sel_hi:[0,1,1]
	s_cmp_lt_i32 s16, 8
	s_cbranch_scc1 .LBB0_1157
.LBB0_1156:
	s_waitcnt vmcnt(16)
	s_waitcnt lgkmcnt(0)
	v_readlane_b32 s14, v176, 7
	v_cvt_pk_f32_fp8_e32 v[4:5], v0
	v_cvt_pk_f32_fp8_sdwa v[6:7], v0 src0_sel:WORD_1
	v_cvt_pk_f32_fp8_e32 v[8:9], v1
	v_cvt_pk_f32_fp8_sdwa v[0:1], v1 src0_sel:WORD_1
	v_pk_fma_f32 v[126:127], v[4:5], s[14:15], v[126:127] op_sel_hi:[1,0,1]
	v_pk_fma_f32 v[124:125], v[6:7], s[14:15], v[124:125] op_sel_hi:[1,0,1]
	v_pk_fma_f32 v[120:121], s[14:15], v[0:1], v[120:121] op_sel_hi:[0,1,1]
	v_cvt_pk_f32_fp8_e32 v[0:1], v2
	v_cvt_pk_f32_fp8_sdwa v[4:5], v2 src0_sel:WORD_1
	v_cvt_pk_f32_fp8_e32 v[6:7], v3
	v_cvt_pk_f32_fp8_sdwa v[2:3], v3 src0_sel:WORD_1
	v_pk_fma_f32 v[122:123], s[14:15], v[8:9], v[122:123] op_sel_hi:[0,1,1]
	v_pk_fma_f32 v[118:119], s[14:15], v[0:1], v[118:119] op_sel_hi:[0,1,1]
	v_pk_fma_f32 v[116:117], s[14:15], v[4:5], v[116:117] op_sel_hi:[0,1,1]
	v_pk_fma_f32 v[114:115], s[14:15], v[6:7], v[114:115] op_sel_hi:[0,1,1]
	v_pk_fma_f32 v[112:113], s[14:15], v[2:3], v[112:113] op_sel_hi:[0,1,1]

.LBB0_1162:
	s_cmp_lt_i32 s16, 2
	s_cbranch_scc1 .LBB0_1305
	s_waitcnt vmcnt(18)
	s_waitcnt lgkmcnt(0)
	v_readlane_b32 s14, v192, 1
	v_cvt_pk_f32_fp8_e32 v[194:195], v56
	v_cvt_pk_f32_fp8_sdwa v[196:197], v56 src0_sel:WORD_1
	v_cvt_pk_f32_fp8_e32 v[198:199], v57
	v_cvt_pk_f32_fp8_sdwa v[200:201], v57 src0_sel:WORD_1
	v_pk_fma_f32 v[188:189], v[194:195], s[14:15], v[188:189] op_sel_hi:[1,0,1]
	v_pk_fma_f32 v[184:185], v[196:197], s[14:15], v[184:185] op_sel_hi:[1,0,1]
	v_pk_fma_f32 v[180:181], s[14:15], v[198:199], v[180:181] op_sel_hi:[0,1,1]
	v_pk_fma_f32 v[176:177], s[14:15], v[200:201], v[176:177] op_sel_hi:[0,1,1]
	v_cvt_pk_f32_fp8_e32 v[194:195], v58
	v_cvt_pk_f32_fp8_sdwa v[196:197], v58 src0_sel:WORD_1
	v_cvt_pk_f32_fp8_e32 v[198:199], v59
	v_cvt_pk_f32_fp8_sdwa v[200:201], v59 src0_sel:WORD_1
	v_pk_fma_f32 v[190:191], s[14:15], v[194:195], v[190:191] op_sel_hi:[0,1,1]
	v_pk_fma_f32 v[186:187], s[14:15], v[196:197], v[186:187] op_sel_hi:[0,1,1]
	v_pk_fma_f32 v[182:183], s[14:15], v[198:199], v[182:183] op_sel_hi:[0,1,1]
	v_pk_fma_f32 v[178:179], s[14:15], v[200:201], v[178:179] op_sel_hi:[0,1,1]
	s_cmp_lt_i32 s16, 3
	s_cbranch_scc0 .LBB0_1306

.LBB0_1165:
	s_waitcnt vmcnt(20)
	s_waitcnt lgkmcnt(0)
	v_readlane_b32 s14, v192, 3
	v_cvt_pk_f32_fp8_e32 v[194:195], v44
	v_cvt_pk_f32_fp8_sdwa v[196:197], v44 src0_sel:WORD_1
	v_cvt_pk_f32_fp8_e32 v[198:199], v45
	v_cvt_pk_f32_fp8_sdwa v[200:201], v45 src0_sel:WORD_1
	v_pk_fma_f32 v[188:189], v[194:195], s[14:15], v[188:189] op_sel_hi:[1,0,1]
	v_pk_fma_f32 v[184:185], v[196:197], s[14:15], v[184:185] op_sel_hi:[1,0,1]
	v_pk_fma_f32 v[180:181], s[14:15], v[198:199], v[180:181] op_sel_hi:[0,1,1]
	v_pk_fma_f32 v[176:177], s[14:15], v[200:201], v[176:177] op_sel_hi:[0,1,1]
	v_cvt_pk_f32_fp8_e32 v[194:195], v46
	v_cvt_pk_f32_fp8_sdwa v[196:197], v46 src0_sel:WORD_1
	v_cvt_pk_f32_fp8_e32 v[198:199], v47
	v_cvt_pk_f32_fp8_sdwa v[200:201], v47 src0_sel:WORD_1
	v_pk_fma_f32 v[190:191], s[14:15], v[194:195], v[190:191] op_sel_hi:[0,1,1]
	v_pk_fma_f32 v[186:187], s[14:15], v[196:197], v[186:187] op_sel_hi:[0,1,1]
	v_pk_fma_f32 v[182:183], s[14:15], v[198:199], v[182:183] op_sel_hi:[0,1,1]
	v_pk_fma_f32 v[178:179], s[14:15], v[200:201], v[178:179] op_sel_hi:[0,1,1]
	s_cmp_lt_i32 s16, 5
	s_cbranch_scc0 .LBB0_1308

.LBB0_1167:
	s_waitcnt vmcnt(17)
	s_waitcnt lgkmcnt(0)
	v_readlane_b32 s14, v192, 5
	v_cvt_pk_f32_fp8_e32 v[194:195], v28
	v_cvt_pk_f32_fp8_sdwa v[196:197], v28 src0_sel:WORD_1
	v_cvt_pk_f32_fp8_e32 v[198:199], v29
	v_cvt_pk_f32_fp8_sdwa v[200:201], v29 src0_sel:WORD_1
	v_pk_fma_f32 v[188:189], v[194:195], s[14:15], v[188:189] op_sel_hi:[1,0,1]
	v_pk_fma_f32 v[184:185], v[196:197], s[14:15], v[184:185] op_sel_hi:[1,0,1]
	v_pk_fma_f32 v[180:181], s[14:15], v[198:199], v[180:181] op_sel_hi:[0,1,1]
	v_pk_fma_f32 v[176:177], s[14:15], v[200:201], v[176:177] op_sel_hi:[0,1,1]
	v_cvt_pk_f32_fp8_e32 v[194:195], v30
	v_cvt_pk_f32_fp8_sdwa v[196:197], v30 src0_sel:WORD_1
	v_cvt_pk_f32_fp8_e32 v[198:199], v31
	v_cvt_pk_f32_fp8_sdwa v[200:201], v31 src0_sel:WORD_1
	v_pk_fma_f32 v[190:191], s[14:15], v[194:195], v[190:191] op_sel_hi:[0,1,1]
	v_pk_fma_f32 v[186:187], s[14:15], v[196:197], v[186:187] op_sel_hi:[0,1,1]
	v_pk_fma_f32 v[182:183], s[14:15], v[198:199], v[182:183] op_sel_hi:[0,1,1]
	v_pk_fma_f32 v[178:179], s[14:15], v[200:201], v[178:179] op_sel_hi:[0,1,1]
	s_cmp_lt_i32 s16, 7
	s_cbranch_scc0 .LBB0_1310

.LBB0_1171:
	s_and_b64 vcc, exec, s[14:15]
	v_mov_b64_e32 v[200:201], v[144:145]
	v_mov_b64_e32 v[204:205], v[146:147]
	v_mov_b64_e32 v[206:207], v[148:149]
	v_mov_b64_e32 v[208:209], v[150:151]
	s_waitcnt lgkmcnt(0)
	v_mov_b64_e32 v[192:193], v[152:153]
	v_mov_b64_e32 v[194:195], v[154:155]
	v_mov_b64_e32 v[196:197], v[156:157]
	v_mov_b64_e32 v[198:199], v[158:159]
	s_cbranch_vccz .LBB0_1183
	v_lshl_add_u32 v176, v234, 2, s17
	ds_read_b32 v176, v176 offset:5120
	s_cmp_lt_i32 s16, 1
	v_mov_b64_e32 v[198:199], v[158:159]
	v_mov_b64_e32 v[196:197], v[156:157]
	v_mov_b64_e32 v[194:195], v[154:155]
	v_mov_b64_e32 v[192:193], v[152:153]
	v_mov_b64_e32 v[208:209], v[150:151]
	v_mov_b64_e32 v[206:207], v[148:149]
	v_mov_b64_e32 v[204:205], v[146:147]
	v_mov_b64_e32 v[200:201], v[144:145]
	s_cbranch_scc1 .LBB0_1174
	s_waitcnt vmcnt(19)
	s_waitcnt lgkmcnt(0)
	v_readlane_b32 s14, v176, 0
	v_cvt_pk_f32_fp8_e32 v[178:179], v60
	v_cvt_pk_f32_fp8_sdwa v[180:181], v60 src0_sel:WORD_1
	v_cvt_pk_f32_fp8_e32 v[182:183], v61
	v_cvt_pk_f32_fp8_sdwa v[184:185], v61 src0_sel:WORD_1
	v_pk_fma_f32 v[198:199], v[178:179], s[14:15], v[158:159] op_sel_hi:[1,0,1]
	v_pk_fma_f32 v[196:197], v[180:181], s[14:15], v[156:157] op_sel_hi:[1,0,1]
	v_pk_fma_f32 v[194:195], s[14:15], v[182:183], v[154:155] op_sel_hi:[0,1,1]
	v_pk_fma_f32 v[192:193], s[14:15], v[184:185], v[152:153] op_sel_hi:[0,1,1]
	v_cvt_pk_f32_fp8_e32 v[178:179], v62
	v_cvt_pk_f32_fp8_sdwa v[180:181], v62 src0_sel:WORD_1
	v_cvt_pk_f32_fp8_e32 v[182:183], v63
	v_cvt_pk_f32_fp8_sdwa v[184:185], v63 src0_sel:WORD_1
	v_pk_fma_f32 v[208:209], s[14:15], v[178:179], v[150:151] op_sel_hi:[0,1,1]
	v_pk_fma_f32 v[206:207], s[14:15], v[180:181], v[148:149] op_sel_hi:[0,1,1]
	v_pk_fma_f32 v[204:205], s[14:15], v[182:183], v[146:147] op_sel_hi:[0,1,1]
	v_pk_fma_f32 v[200:201], s[14:15], v[184:185], v[144:145] op_sel_hi:[0,1,1]
.LBB0_1174:
	s_cmp_lt_i32 s16, 2
	s_cbranch_scc1 .LBB0_1311
	s_waitcnt vmcnt(18)
	s_waitcnt lgkmcnt(0)
	v_readlane_b32 s14, v176, 1
	v_cvt_pk_f32_fp8_e32 v[178:179], v56
	v_cvt_pk_f32_fp8_sdwa v[180:181], v56 src0_sel:WORD_1
	v_cvt_pk_f32_fp8_e32 v[182:183], v57
	v_cvt_pk_f32_fp8_sdwa v[184:185], v57 src0_sel:WORD_1
	v_pk_fma_f32 v[198:199], v[178:179], s[14:15], v[198:199] op_sel_hi:[1,0,1]
	v_pk_fma_f32 v[196:197], v[180:181], s[14:15], v[196:197] op_sel_hi:[1,0,1]
	v_pk_fma_f32 v[194:195], s[14:15], v[182:183], v[194:195] op_sel_hi:[0,1,1]
	v_pk_fma_f32 v[192:193], s[14:15], v[184:185], v[192:193] op_sel_hi:[0,1,1]
	v_cvt_pk_f32_fp8_e32 v[178:179], v58
	v_cvt_pk_f32_fp8_sdwa v[180:181], v58 src0_sel:WORD_1
	v_cvt_pk_f32_fp8_e32 v[182:183], v59
	v_cvt_pk_f32_fp8_sdwa v[184:185], v59 src0_sel:WORD_1
	v_pk_fma_f32 v[208:209], s[14:15], v[178:179], v[208:209] op_sel_hi:[0,1,1]
	v_pk_fma_f32 v[206:207], s[14:15], v[180:181], v[206:207] op_sel_hi:[0,1,1]
	v_pk_fma_f32 v[204:205], s[14:15], v[182:183], v[204:205] op_sel_hi:[0,1,1]
	v_pk_fma_f32 v[200:201], s[14:15], v[184:185], v[200:201] op_sel_hi:[0,1,1]
	s_cmp_lt_i32 s16, 3
	s_cbranch_scc0 .LBB0_1312

.LBB0_1177:
	s_waitcnt vmcnt(20)
	s_waitcnt lgkmcnt(0)
	v_readlane_b32 s14, v176, 3
	v_cvt_pk_f32_fp8_e32 v[178:179], v44
	v_cvt_pk_f32_fp8_sdwa v[180:181], v44 src0_sel:WORD_1
	v_cvt_pk_f32_fp8_e32 v[182:183], v45
	v_cvt_pk_f32_fp8_sdwa v[184:185], v45 src0_sel:WORD_1
	v_pk_fma_f32 v[198:199], v[178:179], s[14:15], v[198:199] op_sel_hi:[1,0,1]
	v_pk_fma_f32 v[196:197], v[180:181], s[14:15], v[196:197] op_sel_hi:[1,0,1]
	v_pk_fma_f32 v[194:195], s[14:15], v[182:183], v[194:195] op_sel_hi:[0,1,1]
	v_pk_fma_f32 v[192:193], s[14:15], v[184:185], v[192:193] op_sel_hi:[0,1,1]
	v_cvt_pk_f32_fp8_e32 v[178:179], v46
	v_cvt_pk_f32_fp8_sdwa v[180:181], v46 src0_sel:WORD_1
	v_cvt_pk_f32_fp8_e32 v[182:183], v47
	v_cvt_pk_f32_fp8_sdwa v[184:185], v47 src0_sel:WORD_1
	v_pk_fma_f32 v[208:209], s[14:15], v[178:179], v[208:209] op_sel_hi:[0,1,1]
	v_pk_fma_f32 v[206:207], s[14:15], v[180:181], v[206:207] op_sel_hi:[0,1,1]
	v_pk_fma_f32 v[204:205], s[14:15], v[182:183], v[204:205] op_sel_hi:[0,1,1]
	v_pk_fma_f32 v[200:201], s[14:15], v[184:185], v[200:201] op_sel_hi:[0,1,1]
	s_cmp_lt_i32 s16, 5
	s_cbranch_scc0 .LBB0_1314

.LBB0_1179:
	s_waitcnt vmcnt(17)
	s_waitcnt lgkmcnt(0)
	v_readlane_b32 s14, v176, 5
	v_cvt_pk_f32_fp8_e32 v[178:179], v28
	v_cvt_pk_f32_fp8_sdwa v[180:181], v28 src0_sel:WORD_1
	v_cvt_pk_f32_fp8_e32 v[182:183], v29
	v_cvt_pk_f32_fp8_sdwa v[184:185], v29 src0_sel:WORD_1
	v_pk_fma_f32 v[198:199], v[178:179], s[14:15], v[198:199] op_sel_hi:[1,0,1]
	v_pk_fma_f32 v[196:197], v[180:181], s[14:15], v[196:197] op_sel_hi:[1,0,1]
	v_pk_fma_f32 v[194:195], s[14:15], v[182:183], v[194:195] op_sel_hi:[0,1,1]
	v_pk_fma_f32 v[192:193], s[14:15], v[184:185], v[192:193] op_sel_hi:[0,1,1]
	v_cvt_pk_f32_fp8_e32 v[178:179], v30
	v_cvt_pk_f32_fp8_sdwa v[180:181], v30 src0_sel:WORD_1
	v_cvt_pk_f32_fp8_e32 v[182:183], v31
	v_cvt_pk_f32_fp8_sdwa v[184:185], v31 src0_sel:WORD_1
	v_pk_fma_f32 v[208:209], s[14:15], v[178:179], v[208:209] op_sel_hi:[0,1,1]
	v_pk_fma_f32 v[206:207], s[14:15], v[180:181], v[206:207] op_sel_hi:[0,1,1]
	v_pk_fma_f32 v[204:205], s[14:15], v[182:183], v[204:205] op_sel_hi:[0,1,1]
	v_pk_fma_f32 v[200:201], s[14:15], v[184:185], v[200:201] op_sel_hi:[0,1,1]
	s_cmp_lt_i32 s16, 7
	s_cbranch_scc0 .LBB0_1316

.LBB0_1184:
	s_andn2_b64 vcc, exec, s[14:15]
	v_mov_b64_e32 v[224:225], v[160:161]
	v_mov_b64_e32 v[222:223], v[162:163]
	v_mov_b64_e32 v[220:221], v[164:165]
	v_mov_b64_e32 v[218:219], v[166:167]
	v_mov_b64_e32 v[216:217], v[168:169]
	v_mov_b64_e32 v[214:215], v[170:171]
	v_mov_b64_e32 v[212:213], v[172:173]
	v_mov_b64_e32 v[210:211], v[174:175]
	s_cbranch_vccnz .LBB0_1196
	v_lshl_add_u32 v176, v234, 2, s17
	ds_read_b32 v176, v176 offset:4608
	s_cmp_lt_i32 s16, 1
	v_mov_b64_e32 v[210:211], v[174:175]
	v_mov_b64_e32 v[212:213], v[172:173]
	v_mov_b64_e32 v[214:215], v[170:171]
	v_mov_b64_e32 v[216:217], v[168:169]
	v_mov_b64_e32 v[218:219], v[166:167]
	v_mov_b64_e32 v[220:221], v[164:165]
	v_mov_b64_e32 v[222:223], v[162:163]
	v_mov_b64_e32 v[224:225], v[160:161]
	s_cbranch_scc1 .LBB0_1187
	s_waitcnt vmcnt(19)
	s_waitcnt lgkmcnt(0)
	v_readlane_b32 s14, v176, 0
	v_cvt_pk_f32_fp8_e32 v[178:179], v60
	v_cvt_pk_f32_fp8_sdwa v[180:181], v60 src0_sel:WORD_1
	v_cvt_pk_f32_fp8_e32 v[182:183], v61
	v_cvt_pk_f32_fp8_sdwa v[184:185], v61 src0_sel:WORD_1
	v_pk_fma_f32 v[210:211], v[178:179], s[14:15], v[174:175] op_sel_hi:[1,0,1]
	v_pk_fma_f32 v[212:213], v[180:181], s[14:15], v[172:173] op_sel_hi:[1,0,1]
	v_pk_fma_f32 v[214:215], s[14:15], v[182:183], v[170:171] op_sel_hi:[0,1,1]
	v_pk_fma_f32 v[216:217], s[14:15], v[184:185], v[168:169] op_sel_hi:[0,1,1]
	v_cvt_pk_f32_fp8_e32 v[178:179], v62
	v_cvt_pk_f32_fp8_sdwa v[180:181], v62 src0_sel:WORD_1
	v_cvt_pk_f32_fp8_e32 v[182:183], v63
	v_cvt_pk_f32_fp8_sdwa v[184:185], v63 src0_sel:WORD_1
	v_pk_fma_f32 v[218:219], s[14:15], v[178:179], v[166:167] op_sel_hi:[0,1,1]
	v_pk_fma_f32 v[220:221], s[14:15], v[180:181], v[164:165] op_sel_hi:[0,1,1]
	v_pk_fma_f32 v[222:223], s[14:15], v[182:183], v[162:163] op_sel_hi:[0,1,1]
	v_pk_fma_f32 v[224:225], s[14:15], v[184:185], v[160:161] op_sel_hi:[0,1,1]
.LBB0_1187:
	s_cmp_lt_i32 s16, 2
	s_cbranch_scc1 .LBB0_1281
	s_waitcnt vmcnt(18)
	s_waitcnt lgkmcnt(0)
	v_readlane_b32 s14, v176, 1
	v_cvt_pk_f32_fp8_e32 v[178:179], v56
	v_cvt_pk_f32_fp8_sdwa v[180:181], v56 src0_sel:WORD_1
	v_cvt_pk_f32_fp8_e32 v[182:183], v57
	v_cvt_pk_f32_fp8_sdwa v[184:185], v57 src0_sel:WORD_1
	v_pk_fma_f32 v[210:211], v[178:179], s[14:15], v[210:211] op_sel_hi:[1,0,1]
	v_pk_fma_f32 v[212:213], v[180:181], s[14:15], v[212:213] op_sel_hi:[1,0,1]
	v_pk_fma_f32 v[214:215], s[14:15], v[182:183], v[214:215] op_sel_hi:[0,1,1]
	v_pk_fma_f32 v[216:217], s[14:15], v[184:185], v[216:217] op_sel_hi:[0,1,1]
	v_cvt_pk_f32_fp8_e32 v[178:179], v58
	v_cvt_pk_f32_fp8_sdwa v[180:181], v58 src0_sel:WORD_1
	v_cvt_pk_f32_fp8_e32 v[182:183], v59
	v_cvt_pk_f32_fp8_sdwa v[184:185], v59 src0_sel:WORD_1
	v_pk_fma_f32 v[218:219], s[14:15], v[178:179], v[218:219] op_sel_hi:[0,1,1]
	v_pk_fma_f32 v[220:221], s[14:15], v[180:181], v[220:221] op_sel_hi:[0,1,1]
	v_pk_fma_f32 v[222:223], s[14:15], v[182:183], v[222:223] op_sel_hi:[0,1,1]
	v_pk_fma_f32 v[224:225], s[14:15], v[184:185], v[224:225] op_sel_hi:[0,1,1]
	s_cmp_lt_i32 s16, 3
	s_cbranch_scc0 .LBB0_1282

.LBB0_1190:
	s_waitcnt vmcnt(20)
	s_waitcnt lgkmcnt(0)
	v_readlane_b32 s14, v176, 3
	v_cvt_pk_f32_fp8_e32 v[178:179], v44
	v_cvt_pk_f32_fp8_sdwa v[180:181], v44 src0_sel:WORD_1
	v_cvt_pk_f32_fp8_e32 v[182:183], v45
	v_cvt_pk_f32_fp8_sdwa v[184:185], v45 src0_sel:WORD_1
	v_pk_fma_f32 v[210:211], v[178:179], s[14:15], v[210:211] op_sel_hi:[1,0,1]
	v_pk_fma_f32 v[212:213], v[180:181], s[14:15], v[212:213] op_sel_hi:[1,0,1]
	v_pk_fma_f32 v[214:215], s[14:15], v[182:183], v[214:215] op_sel_hi:[0,1,1]
	v_pk_fma_f32 v[216:217], s[14:15], v[184:185], v[216:217] op_sel_hi:[0,1,1]
	v_cvt_pk_f32_fp8_e32 v[178:179], v46
	v_cvt_pk_f32_fp8_sdwa v[180:181], v46 src0_sel:WORD_1
	v_cvt_pk_f32_fp8_e32 v[182:183], v47
	v_cvt_pk_f32_fp8_sdwa v[184:185], v47 src0_sel:WORD_1
	v_pk_fma_f32 v[218:219], s[14:15], v[178:179], v[218:219] op_sel_hi:[0,1,1]
	v_pk_fma_f32 v[220:221], s[14:15], v[180:181], v[220:221] op_sel_hi:[0,1,1]
	v_pk_fma_f32 v[222:223], s[14:15], v[182:183], v[222:223] op_sel_hi:[0,1,1]
	v_pk_fma_f32 v[224:225], s[14:15], v[184:185], v[224:225] op_sel_hi:[0,1,1]
	s_cmp_lt_i32 s16, 5
	s_cbranch_scc0 .LBB0_1284

.LBB0_1192:
	s_waitcnt vmcnt(17)
	s_waitcnt lgkmcnt(0)
	v_readlane_b32 s14, v176, 5
	v_cvt_pk_f32_fp8_e32 v[178:179], v28
	v_cvt_pk_f32_fp8_sdwa v[180:181], v28 src0_sel:WORD_1
	v_cvt_pk_f32_fp8_e32 v[182:183], v29
	v_cvt_pk_f32_fp8_sdwa v[184:185], v29 src0_sel:WORD_1
	v_pk_fma_f32 v[210:211], v[178:179], s[14:15], v[210:211] op_sel_hi:[1,0,1]
	v_pk_fma_f32 v[212:213], v[180:181], s[14:15], v[212:213] op_sel_hi:[1,0,1]
	v_pk_fma_f32 v[214:215], s[14:15], v[182:183], v[214:215] op_sel_hi:[0,1,1]
	v_pk_fma_f32 v[216:217], s[14:15], v[184:185], v[216:217] op_sel_hi:[0,1,1]
	v_cvt_pk_f32_fp8_e32 v[178:179], v30
	v_cvt_pk_f32_fp8_sdwa v[180:181], v30 src0_sel:WORD_1
	v_cvt_pk_f32_fp8_e32 v[182:183], v31
	v_cvt_pk_f32_fp8_sdwa v[184:185], v31 src0_sel:WORD_1
	v_pk_fma_f32 v[218:219], s[14:15], v[178:179], v[218:219] op_sel_hi:[0,1,1]
	v_pk_fma_f32 v[220:221], s[14:15], v[180:181], v[220:221] op_sel_hi:[0,1,1]
	v_pk_fma_f32 v[222:223], s[14:15], v[182:183], v[222:223] op_sel_hi:[0,1,1]
	v_pk_fma_f32 v[224:225], s[14:15], v[184:185], v[224:225] op_sel_hi:[0,1,1]
	s_cmp_lt_i32 s16, 7
	s_cbranch_scc0 .LBB0_1286

.LBB0_1197:
	s_andn2_b64 vcc, exec, s[14:15]
	s_cbranch_vccnz .LBB0_1207
	v_lshl_add_u32 v176, v234, 2, s17
	ds_read_b32 v176, v176 offset:4096
	s_cmp_lt_i32 s16, 1
	s_cbranch_scc1 .LBB0_1200
	s_waitcnt vmcnt(19)
	s_waitcnt lgkmcnt(0)
	v_readlane_b32 s14, v176, 0
	v_cvt_pk_f32_fp8_e32 v[178:179], v60
	v_cvt_pk_f32_fp8_sdwa v[180:181], v60 src0_sel:WORD_1
	v_cvt_pk_f32_fp8_e32 v[182:183], v61
	v_cvt_pk_f32_fp8_sdwa v[60:61], v61 src0_sel:WORD_1
	v_pk_fma_f32 v[126:127], v[178:179], s[14:15], v[126:127] op_sel_hi:[1,0,1]
	v_pk_fma_f32 v[124:125], v[180:181], s[14:15], v[124:125] op_sel_hi:[1,0,1]
	v_pk_fma_f32 v[120:121], s[14:15], v[60:61], v[120:121] op_sel_hi:[0,1,1]
	v_cvt_pk_f32_fp8_e32 v[60:61], v62
	v_cvt_pk_f32_fp8_sdwa v[178:179], v62 src0_sel:WORD_1
	v_cvt_pk_f32_fp8_e32 v[180:181], v63
	v_cvt_pk_f32_fp8_sdwa v[62:63], v63 src0_sel:WORD_1
	v_pk_fma_f32 v[122:123], s[14:15], v[182:183], v[122:123] op_sel_hi:[0,1,1]
	v_pk_fma_f32 v[118:119], s[14:15], v[60:61], v[118:119] op_sel_hi:[0,1,1]
	v_pk_fma_f32 v[116:117], s[14:15], v[178:179], v[116:117] op_sel_hi:[0,1,1]
	v_pk_fma_f32 v[114:115], s[14:15], v[180:181], v[114:115] op_sel_hi:[0,1,1]
	v_pk_fma_f32 v[112:113], s[14:15], v[62:63], v[112:113] op_sel_hi:[0,1,1]
.LBB0_1200:
	s_cmp_lt_i32 s16, 2
	s_cbranch_scc1 .LBB0_1208
	s_waitcnt vmcnt(18)
	s_waitcnt lgkmcnt(0)
	v_readlane_b32 s14, v176, 1
	v_cvt_pk_f32_fp8_e32 v[60:61], v56
	v_cvt_pk_f32_fp8_sdwa v[62:63], v56 src0_sel:WORD_1
	v_cvt_pk_f32_fp8_e32 v[178:179], v57
	v_cvt_pk_f32_fp8_sdwa v[56:57], v57 src0_sel:WORD_1
	v_pk_fma_f32 v[126:127], v[60:61], s[14:15], v[126:127] op_sel_hi:[1,0,1]
	v_pk_fma_f32 v[124:125], v[62:63], s[14:15], v[124:125] op_sel_hi:[1,0,1]
	v_pk_fma_f32 v[120:121], s[14:15], v[56:57], v[120:121] op_sel_hi:[0,1,1]
	v_cvt_pk_f32_fp8_e32 v[56:57], v58
	v_cvt_pk_f32_fp8_sdwa v[60:61], v58 src0_sel:WORD_1
	v_cvt_pk_f32_fp8_e32 v[62:63], v59
	v_cvt_pk_f32_fp8_sdwa v[58:59], v59 src0_sel:WORD_1
	v_pk_fma_f32 v[122:123], s[14:15], v[178:179], v[122:123] op_sel_hi:[0,1,1]
	v_pk_fma_f32 v[118:119], s[14:15], v[56:57], v[118:119] op_sel_hi:[0,1,1]
	v_pk_fma_f32 v[116:117], s[14:15], v[60:61], v[116:117] op_sel_hi:[0,1,1]
	v_pk_fma_f32 v[114:115], s[14:15], v[62:63], v[114:115] op_sel_hi:[0,1,1]
	v_pk_fma_f32 v[112:113], s[14:15], v[58:59], v[112:113] op_sel_hi:[0,1,1]
	s_cmp_lt_i32 s16, 3
	s_cbranch_scc0 .LBB0_1209

.LBB0_1203:
	s_waitcnt vmcnt(17)
	s_waitcnt lgkmcnt(0)
	v_readlane_b32 s14, v176, 3
	v_cvt_pk_f32_fp8_e32 v[52:53], v44
	v_cvt_pk_f32_fp8_sdwa v[54:55], v44 src0_sel:WORD_1
	v_cvt_pk_f32_fp8_e32 v[56:57], v45
	v_cvt_pk_f32_fp8_sdwa v[44:45], v45 src0_sel:WORD_1
	v_pk_fma_f32 v[126:127], v[52:53], s[14:15], v[126:127] op_sel_hi:[1,0,1]
	v_pk_fma_f32 v[124:125], v[54:55], s[14:15], v[124:125] op_sel_hi:[1,0,1]
	v_pk_fma_f32 v[120:121], s[14:15], v[44:45], v[120:121] op_sel_hi:[0,1,1]
	v_cvt_pk_f32_fp8_e32 v[44:45], v46
	v_cvt_pk_f32_fp8_sdwa v[52:53], v46 src0_sel:WORD_1
	v_cvt_pk_f32_fp8_e32 v[54:55], v47
	v_cvt_pk_f32_fp8_sdwa v[46:47], v47 src0_sel:WORD_1
	v_pk_fma_f32 v[122:123], s[14:15], v[56:57], v[122:123] op_sel_hi:[0,1,1]
	v_pk_fma_f32 v[118:119], s[14:15], v[44:45], v[118:119] op_sel_hi:[0,1,1]
	v_pk_fma_f32 v[116:117], s[14:15], v[52:53], v[116:117] op_sel_hi:[0,1,1]
	v_pk_fma_f32 v[114:115], s[14:15], v[54:55], v[114:115] op_sel_hi:[0,1,1]
	v_pk_fma_f32 v[112:113], s[14:15], v[46:47], v[112:113] op_sel_hi:[0,1,1]
	s_cmp_lt_i32 s16, 5
	s_cbranch_scc0 .LBB0_1211

.LBB0_1205:
	s_waitcnt vmcnt(17)
	s_waitcnt lgkmcnt(0)
	v_readlane_b32 s14, v176, 5
	v_cvt_pk_f32_fp8_e32 v[40:41], v28
	v_cvt_pk_f32_fp8_sdwa v[42:43], v28 src0_sel:WORD_1
	v_cvt_pk_f32_fp8_e32 v[44:45], v29
	v_cvt_pk_f32_fp8_sdwa v[28:29], v29 src0_sel:WORD_1
	v_pk_fma_f32 v[126:127], v[40:41], s[14:15], v[126:127] op_sel_hi:[1,0,1]
	v_pk_fma_f32 v[124:125], v[42:43], s[14:15], v[124:125] op_sel_hi:[1,0,1]
	v_pk_fma_f32 v[120:121], s[14:15], v[28:29], v[120:121] op_sel_hi:[0,1,1]
	v_cvt_pk_f32_fp8_e32 v[28:29], v30
	v_cvt_pk_f32_fp8_sdwa v[40:41], v30 src0_sel:WORD_1
	v_cvt_pk_f32_fp8_e32 v[42:43], v31
	v_cvt_pk_f32_fp8_sdwa v[30:31], v31 src0_sel:WORD_1
	v_pk_fma_f32 v[122:123], s[14:15], v[44:45], v[122:123] op_sel_hi:[0,1,1]
	v_pk_fma_f32 v[118:119], s[14:15], v[28:29], v[118:119] op_sel_hi:[0,1,1]
	v_pk_fma_f32 v[116:117], s[14:15], v[40:41], v[116:117] op_sel_hi:[0,1,1]
	v_pk_fma_f32 v[114:115], s[14:15], v[42:43], v[114:115] op_sel_hi:[0,1,1]
	v_pk_fma_f32 v[112:113], s[14:15], v[30:31], v[112:113] op_sel_hi:[0,1,1]
	s_cmp_lt_i32 s16, 7
	s_cbranch_scc0 .LBB0_1213

.LBB0_1209:
	s_waitcnt vmcnt(17)
	s_waitcnt lgkmcnt(0)
	v_readlane_b32 s14, v176, 2
	v_cvt_pk_f32_fp8_e32 v[56:57], v52
	v_cvt_pk_f32_fp8_sdwa v[58:59], v52 src0_sel:WORD_1
	v_cvt_pk_f32_fp8_e32 v[60:61], v53
	v_cvt_pk_f32_fp8_sdwa v[52:53], v53 src0_sel:WORD_1
	v_pk_fma_f32 v[126:127], v[56:57], s[14:15], v[126:127] op_sel_hi:[1,0,1]
	v_pk_fma_f32 v[124:125], v[58:59], s[14:15], v[124:125] op_sel_hi:[1,0,1]
	v_pk_fma_f32 v[120:121], s[14:15], v[52:53], v[120:121] op_sel_hi:[0,1,1]
	v_cvt_pk_f32_fp8_e32 v[52:53], v54
	v_cvt_pk_f32_fp8_sdwa v[56:57], v54 src0_sel:WORD_1
	v_cvt_pk_f32_fp8_e32 v[58:59], v55
	v_cvt_pk_f32_fp8_sdwa v[54:55], v55 src0_sel:WORD_1
	v_pk_fma_f32 v[122:123], s[14:15], v[60:61], v[122:123] op_sel_hi:[0,1,1]
	v_pk_fma_f32 v[118:119], s[14:15], v[52:53], v[118:119] op_sel_hi:[0,1,1]
	v_pk_fma_f32 v[116:117], s[14:15], v[56:57], v[116:117] op_sel_hi:[0,1,1]
	v_pk_fma_f32 v[114:115], s[14:15], v[58:59], v[114:115] op_sel_hi:[0,1,1]
	v_pk_fma_f32 v[112:113], s[14:15], v[54:55], v[112:113] op_sel_hi:[0,1,1]
	s_cmp_lt_i32 s16, 4
	s_cbranch_scc0 .LBB0_1203

.LBB0_1213:
	s_waitcnt vmcnt(17)
	s_waitcnt lgkmcnt(0)
	v_readlane_b32 s14, v176, 6
	v_cvt_pk_f32_fp8_e32 v[28:29], v24
	v_cvt_pk_f32_fp8_sdwa v[30:31], v24 src0_sel:WORD_1
	v_cvt_pk_f32_fp8_e32 v[40:41], v25
	v_cvt_pk_f32_fp8_sdwa v[24:25], v25 src0_sel:WORD_1
	v_pk_fma_f32 v[126:127], v[28:29], s[14:15], v[126:127] op_sel_hi:[1,0,1]
	v_pk_fma_f32 v[124:125], v[30:31], s[14:15], v[124:125] op_sel_hi:[1,0,1]
	v_pk_fma_f32 v[120:121], s[14:15], v[24:25], v[120:121] op_sel_hi:[0,1,1]
	v_cvt_pk_f32_fp8_e32 v[24:25], v26
	v_cvt_pk_f32_fp8_sdwa v[28:29], v26 src0_sel:WORD_1
	v_cvt_pk_f32_fp8_e32 v[30:31], v27
	v_cvt_pk_f32_fp8_sdwa v[26:27], v27 src0_sel:WORD_1
	v_pk_fma_f32 v[122:123], s[14:15], v[40:41], v[122:123] op_sel_hi:[0,1,1]
	v_pk_fma_f32 v[118:119], s[14:15], v[24:25], v[118:119] op_sel_hi:[0,1,1]
	v_pk_fma_f32 v[116:117], s[14:15], v[28:29], v[116:117] op_sel_hi:[0,1,1]
	v_pk_fma_f32 v[114:115], s[14:15], v[30:31], v[114:115] op_sel_hi:[0,1,1]
	v_pk_fma_f32 v[112:113], s[14:15], v[26:27], v[112:113] op_sel_hi:[0,1,1]
	s_cmp_lt_i32 s16, 8
	s_cbranch_scc1 .LBB0_1215
.LBB0_1214:
	s_waitcnt vmcnt(16)
	s_waitcnt lgkmcnt(0)
	v_readlane_b32 s14, v176, 7
	v_cvt_pk_f32_fp8_e32 v[24:25], v12
	v_cvt_pk_f32_fp8_sdwa v[26:27], v12 src0_sel:WORD_1
	v_cvt_pk_f32_fp8_e32 v[28:29], v13
	v_cvt_pk_f32_fp8_sdwa v[12:13], v13 src0_sel:WORD_1
	v_pk_fma_f32 v[126:127], v[24:25], s[14:15], v[126:127] op_sel_hi:[1,0,1]
	v_pk_fma_f32 v[124:125], v[26:27], s[14:15], v[124:125] op_sel_hi:[1,0,1]
	v_pk_fma_f32 v[120:121], s[14:15], v[12:13], v[120:121] op_sel_hi:[0,1,1]
	v_cvt_pk_f32_fp8_e32 v[12:13], v14
	v_cvt_pk_f32_fp8_sdwa v[24:25], v14 src0_sel:WORD_1
	v_cvt_pk_f32_fp8_e32 v[26:27], v15
	v_cvt_pk_f32_fp8_sdwa v[14:15], v15 src0_sel:WORD_1
	v_pk_fma_f32 v[122:123], s[14:15], v[28:29], v[122:123] op_sel_hi:[0,1,1]
	v_pk_fma_f32 v[118:119], s[14:15], v[12:13], v[118:119] op_sel_hi:[0,1,1]
	v_pk_fma_f32 v[116:117], s[14:15], v[24:25], v[116:117] op_sel_hi:[0,1,1]
	v_pk_fma_f32 v[114:115], s[14:15], v[26:27], v[114:115] op_sel_hi:[0,1,1]
	v_pk_fma_f32 v[112:113], s[14:15], v[14:15], v[112:113] op_sel_hi:[0,1,1]

.LBB0_1220:
	s_cmp_lt_i32 s16, 2
	s_cbranch_scc1 .LBB0_1317
	s_waitcnt vmcnt(22)
	s_waitcnt lgkmcnt(0)
	v_readlane_b32 s14, v192, 1
	v_cvt_pk_f32_fp8_e32 v[194:195], v88
	v_cvt_pk_f32_fp8_sdwa v[196:197], v88 src0_sel:WORD_1
	v_cvt_pk_f32_fp8_e32 v[198:199], v89
	v_cvt_pk_f32_fp8_sdwa v[200:201], v89 src0_sel:WORD_1
	v_pk_fma_f32 v[188:189], v[194:195], s[14:15], v[188:189] op_sel_hi:[1,0,1]
	v_pk_fma_f32 v[184:185], v[196:197], s[14:15], v[184:185] op_sel_hi:[1,0,1]
	v_pk_fma_f32 v[180:181], s[14:15], v[198:199], v[180:181] op_sel_hi:[0,1,1]
	v_pk_fma_f32 v[176:177], s[14:15], v[200:201], v[176:177] op_sel_hi:[0,1,1]
	v_cvt_pk_f32_fp8_e32 v[194:195], v90
	v_cvt_pk_f32_fp8_sdwa v[196:197], v90 src0_sel:WORD_1
	v_cvt_pk_f32_fp8_e32 v[198:199], v91
	v_cvt_pk_f32_fp8_sdwa v[200:201], v91 src0_sel:WORD_1
	v_pk_fma_f32 v[190:191], s[14:15], v[194:195], v[190:191] op_sel_hi:[0,1,1]
	v_pk_fma_f32 v[186:187], s[14:15], v[196:197], v[186:187] op_sel_hi:[0,1,1]
	v_pk_fma_f32 v[182:183], s[14:15], v[198:199], v[182:183] op_sel_hi:[0,1,1]
	v_pk_fma_f32 v[178:179], s[14:15], v[200:201], v[178:179] op_sel_hi:[0,1,1]
	s_cmp_lt_i32 s16, 3
	s_cbranch_scc0 .LBB0_1318

.LBB0_1223:
	s_waitcnt vmcnt(20)
	s_waitcnt lgkmcnt(0)
	v_readlane_b32 s14, v192, 3
	v_cvt_pk_f32_fp8_e32 v[194:195], v80
	v_cvt_pk_f32_fp8_sdwa v[196:197], v80 src0_sel:WORD_1
	v_cvt_pk_f32_fp8_e32 v[198:199], v81
	v_cvt_pk_f32_fp8_sdwa v[200:201], v81 src0_sel:WORD_1
	v_pk_fma_f32 v[188:189], v[194:195], s[14:15], v[188:189] op_sel_hi:[1,0,1]
	v_pk_fma_f32 v[184:185], v[196:197], s[14:15], v[184:185] op_sel_hi:[1,0,1]
	v_pk_fma_f32 v[180:181], s[14:15], v[198:199], v[180:181] op_sel_hi:[0,1,1]
	v_pk_fma_f32 v[176:177], s[14:15], v[200:201], v[176:177] op_sel_hi:[0,1,1]
	v_cvt_pk_f32_fp8_e32 v[194:195], v82
	v_cvt_pk_f32_fp8_sdwa v[196:197], v82 src0_sel:WORD_1
	v_cvt_pk_f32_fp8_e32 v[198:199], v83
	v_cvt_pk_f32_fp8_sdwa v[200:201], v83 src0_sel:WORD_1
	v_pk_fma_f32 v[190:191], s[14:15], v[194:195], v[190:191] op_sel_hi:[0,1,1]
	v_pk_fma_f32 v[186:187], s[14:15], v[196:197], v[186:187] op_sel_hi:[0,1,1]
	v_pk_fma_f32 v[182:183], s[14:15], v[198:199], v[182:183] op_sel_hi:[0,1,1]
	v_pk_fma_f32 v[178:179], s[14:15], v[200:201], v[178:179] op_sel_hi:[0,1,1]
	s_cmp_lt_i32 s16, 5
	s_cbranch_scc0 .LBB0_1320

.LBB0_1225:
	s_waitcnt vmcnt(18)
	s_waitcnt lgkmcnt(0)
	v_readlane_b32 s14, v192, 5
	v_cvt_pk_f32_fp8_e32 v[194:195], v72
	v_cvt_pk_f32_fp8_sdwa v[196:197], v72 src0_sel:WORD_1
	v_cvt_pk_f32_fp8_e32 v[198:199], v73
	v_cvt_pk_f32_fp8_sdwa v[200:201], v73 src0_sel:WORD_1
	v_pk_fma_f32 v[188:189], v[194:195], s[14:15], v[188:189] op_sel_hi:[1,0,1]
	v_pk_fma_f32 v[184:185], v[196:197], s[14:15], v[184:185] op_sel_hi:[1,0,1]
	v_pk_fma_f32 v[180:181], s[14:15], v[198:199], v[180:181] op_sel_hi:[0,1,1]
	v_pk_fma_f32 v[176:177], s[14:15], v[200:201], v[176:177] op_sel_hi:[0,1,1]
	v_cvt_pk_f32_fp8_e32 v[194:195], v74
	v_cvt_pk_f32_fp8_sdwa v[196:197], v74 src0_sel:WORD_1
	v_cvt_pk_f32_fp8_e32 v[198:199], v75
	v_cvt_pk_f32_fp8_sdwa v[200:201], v75 src0_sel:WORD_1
	v_pk_fma_f32 v[190:191], s[14:15], v[194:195], v[190:191] op_sel_hi:[0,1,1]
	v_pk_fma_f32 v[186:187], s[14:15], v[196:197], v[186:187] op_sel_hi:[0,1,1]
	v_pk_fma_f32 v[182:183], s[14:15], v[198:199], v[182:183] op_sel_hi:[0,1,1]
	v_pk_fma_f32 v[178:179], s[14:15], v[200:201], v[178:179] op_sel_hi:[0,1,1]
	s_cmp_lt_i32 s16, 7
	s_cbranch_scc0 .LBB0_1322

.LBB0_1229:
	s_and_b64 vcc, exec, s[14:15]
	v_mov_b64_e32 v[200:201], v[144:145]
	v_mov_b64_e32 v[204:205], v[146:147]
	v_mov_b64_e32 v[206:207], v[148:149]
	v_mov_b64_e32 v[208:209], v[150:151]
	s_waitcnt lgkmcnt(0)
	v_mov_b64_e32 v[192:193], v[152:153]
	v_mov_b64_e32 v[194:195], v[154:155]
	v_mov_b64_e32 v[196:197], v[156:157]
	v_mov_b64_e32 v[198:199], v[158:159]
	s_cbranch_vccz .LBB0_1241
	v_lshl_add_u32 v176, v234, 2, s17
	ds_read_b32 v176, v176 offset:5120
	s_cmp_lt_i32 s16, 1
	v_mov_b64_e32 v[198:199], v[158:159]
	v_mov_b64_e32 v[196:197], v[156:157]
	v_mov_b64_e32 v[194:195], v[154:155]
	v_mov_b64_e32 v[192:193], v[152:153]
	v_mov_b64_e32 v[208:209], v[150:151]
	v_mov_b64_e32 v[206:207], v[148:149]
	v_mov_b64_e32 v[204:205], v[146:147]
	v_mov_b64_e32 v[200:201], v[144:145]
	s_cbranch_scc1 .LBB0_1232
	s_waitcnt vmcnt(23)
	s_waitcnt lgkmcnt(0)
	v_readlane_b32 s14, v176, 0
	v_cvt_pk_f32_fp8_e32 v[178:179], v92
	v_cvt_pk_f32_fp8_sdwa v[180:181], v92 src0_sel:WORD_1
	v_cvt_pk_f32_fp8_e32 v[182:183], v93
	v_cvt_pk_f32_fp8_sdwa v[184:185], v93 src0_sel:WORD_1
	v_pk_fma_f32 v[198:199], v[178:179], s[14:15], v[158:159] op_sel_hi:[1,0,1]
	v_pk_fma_f32 v[196:197], v[180:181], s[14:15], v[156:157] op_sel_hi:[1,0,1]
	v_pk_fma_f32 v[194:195], s[14:15], v[182:183], v[154:155] op_sel_hi:[0,1,1]
	v_pk_fma_f32 v[192:193], s[14:15], v[184:185], v[152:153] op_sel_hi:[0,1,1]
	v_cvt_pk_f32_fp8_e32 v[178:179], v94
	v_cvt_pk_f32_fp8_sdwa v[180:181], v94 src0_sel:WORD_1
	v_cvt_pk_f32_fp8_e32 v[182:183], v95
	v_cvt_pk_f32_fp8_sdwa v[184:185], v95 src0_sel:WORD_1
	v_pk_fma_f32 v[208:209], s[14:15], v[178:179], v[150:151] op_sel_hi:[0,1,1]
	v_pk_fma_f32 v[206:207], s[14:15], v[180:181], v[148:149] op_sel_hi:[0,1,1]
	v_pk_fma_f32 v[204:205], s[14:15], v[182:183], v[146:147] op_sel_hi:[0,1,1]
	v_pk_fma_f32 v[200:201], s[14:15], v[184:185], v[144:145] op_sel_hi:[0,1,1]
.LBB0_1232:
	s_cmp_lt_i32 s16, 2
	s_cbranch_scc1 .LBB0_1323
	s_waitcnt vmcnt(22)
	s_waitcnt lgkmcnt(0)
	v_readlane_b32 s14, v176, 1
	v_cvt_pk_f32_fp8_e32 v[178:179], v88
	v_cvt_pk_f32_fp8_sdwa v[180:181], v88 src0_sel:WORD_1
	v_cvt_pk_f32_fp8_e32 v[182:183], v89
	v_cvt_pk_f32_fp8_sdwa v[184:185], v89 src0_sel:WORD_1
	v_pk_fma_f32 v[198:199], v[178:179], s[14:15], v[198:199] op_sel_hi:[1,0,1]
	v_pk_fma_f32 v[196:197], v[180:181], s[14:15], v[196:197] op_sel_hi:[1,0,1]
	v_pk_fma_f32 v[194:195], s[14:15], v[182:183], v[194:195] op_sel_hi:[0,1,1]
	v_pk_fma_f32 v[192:193], s[14:15], v[184:185], v[192:193] op_sel_hi:[0,1,1]
	v_cvt_pk_f32_fp8_e32 v[178:179], v90
	v_cvt_pk_f32_fp8_sdwa v[180:181], v90 src0_sel:WORD_1
	v_cvt_pk_f32_fp8_e32 v[182:183], v91
	v_cvt_pk_f32_fp8_sdwa v[184:185], v91 src0_sel:WORD_1
	v_pk_fma_f32 v[208:209], s[14:15], v[178:179], v[208:209] op_sel_hi:[0,1,1]
	v_pk_fma_f32 v[206:207], s[14:15], v[180:181], v[206:207] op_sel_hi:[0,1,1]
	v_pk_fma_f32 v[204:205], s[14:15], v[182:183], v[204:205] op_sel_hi:[0,1,1]
	v_pk_fma_f32 v[200:201], s[14:15], v[184:185], v[200:201] op_sel_hi:[0,1,1]
	s_cmp_lt_i32 s16, 3
	s_cbranch_scc0 .LBB0_1324

.LBB0_1235:
	s_waitcnt vmcnt(20)
	s_waitcnt lgkmcnt(0)
	v_readlane_b32 s14, v176, 3
	v_cvt_pk_f32_fp8_e32 v[178:179], v80
	v_cvt_pk_f32_fp8_sdwa v[180:181], v80 src0_sel:WORD_1
	v_cvt_pk_f32_fp8_e32 v[182:183], v81
	v_cvt_pk_f32_fp8_sdwa v[184:185], v81 src0_sel:WORD_1
	v_pk_fma_f32 v[198:199], v[178:179], s[14:15], v[198:199] op_sel_hi:[1,0,1]
	v_pk_fma_f32 v[196:197], v[180:181], s[14:15], v[196:197] op_sel_hi:[1,0,1]
	v_pk_fma_f32 v[194:195], s[14:15], v[182:183], v[194:195] op_sel_hi:[0,1,1]
	v_pk_fma_f32 v[192:193], s[14:15], v[184:185], v[192:193] op_sel_hi:[0,1,1]
	v_cvt_pk_f32_fp8_e32 v[178:179], v82
	v_cvt_pk_f32_fp8_sdwa v[180:181], v82 src0_sel:WORD_1
	v_cvt_pk_f32_fp8_e32 v[182:183], v83
	v_cvt_pk_f32_fp8_sdwa v[184:185], v83 src0_sel:WORD_1
	v_pk_fma_f32 v[208:209], s[14:15], v[178:179], v[208:209] op_sel_hi:[0,1,1]
	v_pk_fma_f32 v[206:207], s[14:15], v[180:181], v[206:207] op_sel_hi:[0,1,1]
	v_pk_fma_f32 v[204:205], s[14:15], v[182:183], v[204:205] op_sel_hi:[0,1,1]
	v_pk_fma_f32 v[200:201], s[14:15], v[184:185], v[200:201] op_sel_hi:[0,1,1]
	s_cmp_lt_i32 s16, 5
	s_cbranch_scc0 .LBB0_1326

.LBB0_1237:
	s_waitcnt vmcnt(18)
	s_waitcnt lgkmcnt(0)
	v_readlane_b32 s14, v176, 5
	v_cvt_pk_f32_fp8_e32 v[178:179], v72
	v_cvt_pk_f32_fp8_sdwa v[180:181], v72 src0_sel:WORD_1
	v_cvt_pk_f32_fp8_e32 v[182:183], v73
	v_cvt_pk_f32_fp8_sdwa v[184:185], v73 src0_sel:WORD_1
	v_pk_fma_f32 v[198:199], v[178:179], s[14:15], v[198:199] op_sel_hi:[1,0,1]
	v_pk_fma_f32 v[196:197], v[180:181], s[14:15], v[196:197] op_sel_hi:[1,0,1]
	v_pk_fma_f32 v[194:195], s[14:15], v[182:183], v[194:195] op_sel_hi:[0,1,1]
	v_pk_fma_f32 v[192:193], s[14:15], v[184:185], v[192:193] op_sel_hi:[0,1,1]
	v_cvt_pk_f32_fp8_e32 v[178:179], v74
	v_cvt_pk_f32_fp8_sdwa v[180:181], v74 src0_sel:WORD_1
	v_cvt_pk_f32_fp8_e32 v[182:183], v75
	v_cvt_pk_f32_fp8_sdwa v[184:185], v75 src0_sel:WORD_1
	v_pk_fma_f32 v[208:209], s[14:15], v[178:179], v[208:209] op_sel_hi:[0,1,1]
	v_pk_fma_f32 v[206:207], s[14:15], v[180:181], v[206:207] op_sel_hi:[0,1,1]
	v_pk_fma_f32 v[204:205], s[14:15], v[182:183], v[204:205] op_sel_hi:[0,1,1]
	v_pk_fma_f32 v[200:201], s[14:15], v[184:185], v[200:201] op_sel_hi:[0,1,1]
	s_cmp_lt_i32 s16, 7
	s_cbranch_scc0 .LBB0_1328

.LBB0_1242:
	s_andn2_b64 vcc, exec, s[14:15]
	v_mov_b64_e32 v[224:225], v[160:161]
	v_mov_b64_e32 v[222:223], v[162:163]
	v_mov_b64_e32 v[220:221], v[164:165]
	v_mov_b64_e32 v[218:219], v[166:167]
	v_mov_b64_e32 v[216:217], v[168:169]
	v_mov_b64_e32 v[214:215], v[170:171]
	v_mov_b64_e32 v[212:213], v[172:173]
	v_mov_b64_e32 v[210:211], v[174:175]
	s_cbranch_vccnz .LBB0_1254
	v_lshl_add_u32 v176, v234, 2, s17
	ds_read_b32 v176, v176 offset:4608
	s_cmp_lt_i32 s16, 1
	v_mov_b64_e32 v[210:211], v[174:175]
	v_mov_b64_e32 v[212:213], v[172:173]
	v_mov_b64_e32 v[214:215], v[170:171]
	v_mov_b64_e32 v[216:217], v[168:169]
	v_mov_b64_e32 v[218:219], v[166:167]
	v_mov_b64_e32 v[220:221], v[164:165]
	v_mov_b64_e32 v[222:223], v[162:163]
	v_mov_b64_e32 v[224:225], v[160:161]
	s_cbranch_scc1 .LBB0_1245
	s_waitcnt vmcnt(23)
	s_waitcnt lgkmcnt(0)
	v_readlane_b32 s14, v176, 0
	v_cvt_pk_f32_fp8_e32 v[178:179], v92
	v_cvt_pk_f32_fp8_sdwa v[180:181], v92 src0_sel:WORD_1
	v_cvt_pk_f32_fp8_e32 v[182:183], v93
	v_cvt_pk_f32_fp8_sdwa v[184:185], v93 src0_sel:WORD_1
	v_pk_fma_f32 v[210:211], v[178:179], s[14:15], v[174:175] op_sel_hi:[1,0,1]
	v_pk_fma_f32 v[212:213], v[180:181], s[14:15], v[172:173] op_sel_hi:[1,0,1]
	v_pk_fma_f32 v[214:215], s[14:15], v[182:183], v[170:171] op_sel_hi:[0,1,1]
	v_pk_fma_f32 v[216:217], s[14:15], v[184:185], v[168:169] op_sel_hi:[0,1,1]
	v_cvt_pk_f32_fp8_e32 v[178:179], v94
	v_cvt_pk_f32_fp8_sdwa v[180:181], v94 src0_sel:WORD_1
	v_cvt_pk_f32_fp8_e32 v[182:183], v95
	v_cvt_pk_f32_fp8_sdwa v[184:185], v95 src0_sel:WORD_1
	v_pk_fma_f32 v[218:219], s[14:15], v[178:179], v[166:167] op_sel_hi:[0,1,1]
	v_pk_fma_f32 v[220:221], s[14:15], v[180:181], v[164:165] op_sel_hi:[0,1,1]
	v_pk_fma_f32 v[222:223], s[14:15], v[182:183], v[162:163] op_sel_hi:[0,1,1]
	v_pk_fma_f32 v[224:225], s[14:15], v[184:185], v[160:161] op_sel_hi:[0,1,1]
.LBB0_1245:
	s_cmp_lt_i32 s16, 2
	s_cbranch_scc1 .LBB0_1287
	s_waitcnt vmcnt(22)
	s_waitcnt lgkmcnt(0)
	v_readlane_b32 s14, v176, 1
	v_cvt_pk_f32_fp8_e32 v[178:179], v88
	v_cvt_pk_f32_fp8_sdwa v[180:181], v88 src0_sel:WORD_1
	v_cvt_pk_f32_fp8_e32 v[182:183], v89
	v_cvt_pk_f32_fp8_sdwa v[184:185], v89 src0_sel:WORD_1
	v_pk_fma_f32 v[210:211], v[178:179], s[14:15], v[210:211] op_sel_hi:[1,0,1]
	v_pk_fma_f32 v[212:213], v[180:181], s[14:15], v[212:213] op_sel_hi:[1,0,1]
	v_pk_fma_f32 v[214:215], s[14:15], v[182:183], v[214:215] op_sel_hi:[0,1,1]
	v_pk_fma_f32 v[216:217], s[14:15], v[184:185], v[216:217] op_sel_hi:[0,1,1]
	v_cvt_pk_f32_fp8_e32 v[178:179], v90
	v_cvt_pk_f32_fp8_sdwa v[180:181], v90 src0_sel:WORD_1
	v_cvt_pk_f32_fp8_e32 v[182:183], v91
	v_cvt_pk_f32_fp8_sdwa v[184:185], v91 src0_sel:WORD_1
	v_pk_fma_f32 v[218:219], s[14:15], v[178:179], v[218:219] op_sel_hi:[0,1,1]
	v_pk_fma_f32 v[220:221], s[14:15], v[180:181], v[220:221] op_sel_hi:[0,1,1]
	v_pk_fma_f32 v[222:223], s[14:15], v[182:183], v[222:223] op_sel_hi:[0,1,1]
	v_pk_fma_f32 v[224:225], s[14:15], v[184:185], v[224:225] op_sel_hi:[0,1,1]
	s_cmp_lt_i32 s16, 3
	s_cbranch_scc0 .LBB0_1288

.LBB0_1248:
	s_waitcnt vmcnt(20)
	s_waitcnt lgkmcnt(0)
	v_readlane_b32 s14, v176, 3
	v_cvt_pk_f32_fp8_e32 v[178:179], v80
	v_cvt_pk_f32_fp8_sdwa v[180:181], v80 src0_sel:WORD_1
	v_cvt_pk_f32_fp8_e32 v[182:183], v81
	v_cvt_pk_f32_fp8_sdwa v[184:185], v81 src0_sel:WORD_1
	v_pk_fma_f32 v[210:211], v[178:179], s[14:15], v[210:211] op_sel_hi:[1,0,1]
	v_pk_fma_f32 v[212:213], v[180:181], s[14:15], v[212:213] op_sel_hi:[1,0,1]
	v_pk_fma_f32 v[214:215], s[14:15], v[182:183], v[214:215] op_sel_hi:[0,1,1]
	v_pk_fma_f32 v[216:217], s[14:15], v[184:185], v[216:217] op_sel_hi:[0,1,1]
	v_cvt_pk_f32_fp8_e32 v[178:179], v82
	v_cvt_pk_f32_fp8_sdwa v[180:181], v82 src0_sel:WORD_1
	v_cvt_pk_f32_fp8_e32 v[182:183], v83
	v_cvt_pk_f32_fp8_sdwa v[184:185], v83 src0_sel:WORD_1
	v_pk_fma_f32 v[218:219], s[14:15], v[178:179], v[218:219] op_sel_hi:[0,1,1]
	v_pk_fma_f32 v[220:221], s[14:15], v[180:181], v[220:221] op_sel_hi:[0,1,1]
	v_pk_fma_f32 v[222:223], s[14:15], v[182:183], v[222:223] op_sel_hi:[0,1,1]
	v_pk_fma_f32 v[224:225], s[14:15], v[184:185], v[224:225] op_sel_hi:[0,1,1]
	s_cmp_lt_i32 s16, 5
	s_cbranch_scc0 .LBB0_1290

.LBB0_1250:
	s_waitcnt vmcnt(18)
	s_waitcnt lgkmcnt(0)
	v_readlane_b32 s14, v176, 5
	v_cvt_pk_f32_fp8_e32 v[178:179], v72
	v_cvt_pk_f32_fp8_sdwa v[180:181], v72 src0_sel:WORD_1
	v_cvt_pk_f32_fp8_e32 v[182:183], v73
	v_cvt_pk_f32_fp8_sdwa v[184:185], v73 src0_sel:WORD_1
	v_pk_fma_f32 v[210:211], v[178:179], s[14:15], v[210:211] op_sel_hi:[1,0,1]
	v_pk_fma_f32 v[212:213], v[180:181], s[14:15], v[212:213] op_sel_hi:[1,0,1]
	v_pk_fma_f32 v[214:215], s[14:15], v[182:183], v[214:215] op_sel_hi:[0,1,1]
	v_pk_fma_f32 v[216:217], s[14:15], v[184:185], v[216:217] op_sel_hi:[0,1,1]
	v_cvt_pk_f32_fp8_e32 v[178:179], v74
	v_cvt_pk_f32_fp8_sdwa v[180:181], v74 src0_sel:WORD_1
	v_cvt_pk_f32_fp8_e32 v[182:183], v75
	v_cvt_pk_f32_fp8_sdwa v[184:185], v75 src0_sel:WORD_1
	v_pk_fma_f32 v[218:219], s[14:15], v[178:179], v[218:219] op_sel_hi:[0,1,1]
	v_pk_fma_f32 v[220:221], s[14:15], v[180:181], v[220:221] op_sel_hi:[0,1,1]
	v_pk_fma_f32 v[222:223], s[14:15], v[182:183], v[222:223] op_sel_hi:[0,1,1]
	v_pk_fma_f32 v[224:225], s[14:15], v[184:185], v[224:225] op_sel_hi:[0,1,1]
	s_cmp_lt_i32 s16, 7
	s_cbranch_scc0 .LBB0_1292

.LBB0_1255:
	s_andn2_b64 vcc, exec, s[14:15]
	s_cbranch_vccnz .LBB0_1266
	v_lshl_add_u32 v176, v234, 2, s17
	ds_read_b32 v176, v176 offset:4096
	s_cmp_lt_i32 s16, 1
	s_cbranch_scc1 .LBB0_1258
	s_waitcnt vmcnt(23)
	s_waitcnt lgkmcnt(0)
	v_readlane_b32 s14, v176, 0
	v_cvt_pk_f32_fp8_e32 v[178:179], v92
	v_cvt_pk_f32_fp8_sdwa v[180:181], v92 src0_sel:WORD_1
	v_cvt_pk_f32_fp8_e32 v[182:183], v93
	v_cvt_pk_f32_fp8_sdwa v[92:93], v93 src0_sel:WORD_1
	v_pk_fma_f32 v[126:127], v[178:179], s[14:15], v[126:127] op_sel_hi:[1,0,1]
	v_pk_fma_f32 v[124:125], v[180:181], s[14:15], v[124:125] op_sel_hi:[1,0,1]
	v_pk_fma_f32 v[120:121], s[14:15], v[92:93], v[120:121] op_sel_hi:[0,1,1]
	v_cvt_pk_f32_fp8_e32 v[92:93], v94
	v_cvt_pk_f32_fp8_sdwa v[178:179], v94 src0_sel:WORD_1
	v_cvt_pk_f32_fp8_e32 v[180:181], v95
	v_cvt_pk_f32_fp8_sdwa v[94:95], v95 src0_sel:WORD_1
	v_pk_fma_f32 v[122:123], s[14:15], v[182:183], v[122:123] op_sel_hi:[0,1,1]
	v_pk_fma_f32 v[118:119], s[14:15], v[92:93], v[118:119] op_sel_hi:[0,1,1]
	v_pk_fma_f32 v[116:117], s[14:15], v[178:179], v[116:117] op_sel_hi:[0,1,1]
	v_pk_fma_f32 v[114:115], s[14:15], v[180:181], v[114:115] op_sel_hi:[0,1,1]
	v_pk_fma_f32 v[112:113], s[14:15], v[94:95], v[112:113] op_sel_hi:[0,1,1]
.LBB0_1258:
	s_cmp_lt_i32 s16, 2
	s_cbranch_scc1 .LBB0_1267
	s_waitcnt vmcnt(22)
	s_waitcnt lgkmcnt(0)
	v_readlane_b32 s14, v176, 1
	v_cvt_pk_f32_fp8_e32 v[92:93], v88
	v_cvt_pk_f32_fp8_sdwa v[94:95], v88 src0_sel:WORD_1
	v_cvt_pk_f32_fp8_e32 v[178:179], v89
	v_cvt_pk_f32_fp8_sdwa v[88:89], v89 src0_sel:WORD_1
	v_pk_fma_f32 v[126:127], v[92:93], s[14:15], v[126:127] op_sel_hi:[1,0,1]
	v_pk_fma_f32 v[124:125], v[94:95], s[14:15], v[124:125] op_sel_hi:[1,0,1]
	v_pk_fma_f32 v[120:121], s[14:15], v[88:89], v[120:121] op_sel_hi:[0,1,1]
	v_cvt_pk_f32_fp8_e32 v[88:89], v90
	v_cvt_pk_f32_fp8_sdwa v[92:93], v90 src0_sel:WORD_1
	v_cvt_pk_f32_fp8_e32 v[94:95], v91
	v_cvt_pk_f32_fp8_sdwa v[90:91], v91 src0_sel:WORD_1
	v_pk_fma_f32 v[122:123], s[14:15], v[178:179], v[122:123] op_sel_hi:[0,1,1]
	v_pk_fma_f32 v[118:119], s[14:15], v[88:89], v[118:119] op_sel_hi:[0,1,1]
	v_pk_fma_f32 v[116:117], s[14:15], v[92:93], v[116:117] op_sel_hi:[0,1,1]
	v_pk_fma_f32 v[114:115], s[14:15], v[94:95], v[114:115] op_sel_hi:[0,1,1]
	v_pk_fma_f32 v[112:113], s[14:15], v[90:91], v[112:113] op_sel_hi:[0,1,1]
	s_cmp_lt_i32 s16, 3
	s_cbranch_scc0 .LBB0_1268

.LBB0_1261:
	s_waitcnt vmcnt(20)
	s_waitcnt lgkmcnt(0)
	v_readlane_b32 s14, v176, 3
	v_cvt_pk_f32_fp8_e32 v[84:85], v80
	v_cvt_pk_f32_fp8_sdwa v[86:87], v80 src0_sel:WORD_1
	v_cvt_pk_f32_fp8_e32 v[88:89], v81
	v_cvt_pk_f32_fp8_sdwa v[80:81], v81 src0_sel:WORD_1
	v_pk_fma_f32 v[126:127], v[84:85], s[14:15], v[126:127] op_sel_hi:[1,0,1]
	v_pk_fma_f32 v[124:125], v[86:87], s[14:15], v[124:125] op_sel_hi:[1,0,1]
	v_pk_fma_f32 v[120:121], s[14:15], v[80:81], v[120:121] op_sel_hi:[0,1,1]
	v_cvt_pk_f32_fp8_e32 v[80:81], v82
	v_cvt_pk_f32_fp8_sdwa v[84:85], v82 src0_sel:WORD_1
	v_cvt_pk_f32_fp8_e32 v[86:87], v83
	v_cvt_pk_f32_fp8_sdwa v[82:83], v83 src0_sel:WORD_1
	v_pk_fma_f32 v[122:123], s[14:15], v[88:89], v[122:123] op_sel_hi:[0,1,1]
	v_pk_fma_f32 v[118:119], s[14:15], v[80:81], v[118:119] op_sel_hi:[0,1,1]
	v_pk_fma_f32 v[116:117], s[14:15], v[84:85], v[116:117] op_sel_hi:[0,1,1]
	v_pk_fma_f32 v[114:115], s[14:15], v[86:87], v[114:115] op_sel_hi:[0,1,1]
	v_pk_fma_f32 v[112:113], s[14:15], v[82:83], v[112:113] op_sel_hi:[0,1,1]
	s_cmp_lt_i32 s16, 5
	s_cbranch_scc0 .LBB0_1270

.LBB0_1263:
	s_waitcnt vmcnt(18)
	s_waitcnt lgkmcnt(0)
	v_readlane_b32 s14, v176, 5
	v_cvt_pk_f32_fp8_e32 v[76:77], v72
	v_cvt_pk_f32_fp8_sdwa v[78:79], v72 src0_sel:WORD_1
	v_cvt_pk_f32_fp8_e32 v[80:81], v73
	v_cvt_pk_f32_fp8_sdwa v[72:73], v73 src0_sel:WORD_1
	v_pk_fma_f32 v[126:127], v[76:77], s[14:15], v[126:127] op_sel_hi:[1,0,1]
	v_pk_fma_f32 v[124:125], v[78:79], s[14:15], v[124:125] op_sel_hi:[1,0,1]
	v_pk_fma_f32 v[120:121], s[14:15], v[72:73], v[120:121] op_sel_hi:[0,1,1]
	v_cvt_pk_f32_fp8_e32 v[72:73], v74
	v_cvt_pk_f32_fp8_sdwa v[76:77], v74 src0_sel:WORD_1
	v_cvt_pk_f32_fp8_e32 v[78:79], v75
	v_cvt_pk_f32_fp8_sdwa v[74:75], v75 src0_sel:WORD_1
	v_pk_fma_f32 v[122:123], s[14:15], v[80:81], v[122:123] op_sel_hi:[0,1,1]
	v_pk_fma_f32 v[118:119], s[14:15], v[72:73], v[118:119] op_sel_hi:[0,1,1]
	v_pk_fma_f32 v[116:117], s[14:15], v[76:77], v[116:117] op_sel_hi:[0,1,1]
	v_pk_fma_f32 v[114:115], s[14:15], v[78:79], v[114:115] op_sel_hi:[0,1,1]
	v_pk_fma_f32 v[112:113], s[14:15], v[74:75], v[112:113] op_sel_hi:[0,1,1]
	s_cmp_lt_i32 s16, 7
	s_cbranch_scc0 .LBB0_1272

.LBB0_1265:
	s_waitcnt vmcnt(16)
	s_waitcnt lgkmcnt(0)
	v_readlane_b32 s14, v176, 7
	v_cvt_pk_f32_fp8_e32 v[68:69], v64
	v_cvt_pk_f32_fp8_sdwa v[70:71], v64 src0_sel:WORD_1
	v_cvt_pk_f32_fp8_e32 v[72:73], v65
	v_cvt_pk_f32_fp8_sdwa v[64:65], v65 src0_sel:WORD_1
	v_pk_fma_f32 v[126:127], v[68:69], s[14:15], v[126:127] op_sel_hi:[1,0,1]
	v_pk_fma_f32 v[124:125], v[70:71], s[14:15], v[124:125] op_sel_hi:[1,0,1]
	v_pk_fma_f32 v[120:121], s[14:15], v[64:65], v[120:121] op_sel_hi:[0,1,1]
	v_cvt_pk_f32_fp8_e32 v[64:65], v66
	v_cvt_pk_f32_fp8_sdwa v[68:69], v66 src0_sel:WORD_1
	v_cvt_pk_f32_fp8_e32 v[70:71], v67
	v_cvt_pk_f32_fp8_sdwa v[66:67], v67 src0_sel:WORD_1
	v_pk_fma_f32 v[122:123], s[14:15], v[72:73], v[122:123] op_sel_hi:[0,1,1]
	v_pk_fma_f32 v[118:119], s[14:15], v[64:65], v[118:119] op_sel_hi:[0,1,1]
	v_pk_fma_f32 v[116:117], s[14:15], v[68:69], v[116:117] op_sel_hi:[0,1,1]
	v_pk_fma_f32 v[114:115], s[14:15], v[70:71], v[114:115] op_sel_hi:[0,1,1]
	v_pk_fma_f32 v[112:113], s[14:15], v[66:67], v[112:113] op_sel_hi:[0,1,1]
	s_add_i32 s29, s29, 3
	s_cmp_ge_i32 s29, s49
	s_cbranch_scc0 .LBB0_1274
	s_branch .LBB0_1329

.LBB0_1268:
	s_waitcnt vmcnt(21)
	s_waitcnt lgkmcnt(0)
	v_readlane_b32 s14, v176, 2
	v_cvt_pk_f32_fp8_e32 v[88:89], v84
	v_cvt_pk_f32_fp8_sdwa v[90:91], v84 src0_sel:WORD_1
	v_cvt_pk_f32_fp8_e32 v[92:93], v85
	v_cvt_pk_f32_fp8_sdwa v[84:85], v85 src0_sel:WORD_1
	v_pk_fma_f32 v[126:127], v[88:89], s[14:15], v[126:127] op_sel_hi:[1,0,1]
	v_pk_fma_f32 v[124:125], v[90:91], s[14:15], v[124:125] op_sel_hi:[1,0,1]
	v_pk_fma_f32 v[120:121], s[14:15], v[84:85], v[120:121] op_sel_hi:[0,1,1]
	v_cvt_pk_f32_fp8_e32 v[84:85], v86
	v_cvt_pk_f32_fp8_sdwa v[88:89], v86 src0_sel:WORD_1
	v_cvt_pk_f32_fp8_e32 v[90:91], v87
	v_cvt_pk_f32_fp8_sdwa v[86:87], v87 src0_sel:WORD_1
	v_pk_fma_f32 v[122:123], s[14:15], v[92:93], v[122:123] op_sel_hi:[0,1,1]
	v_pk_fma_f32 v[118:119], s[14:15], v[84:85], v[118:119] op_sel_hi:[0,1,1]
	v_pk_fma_f32 v[116:117], s[14:15], v[88:89], v[116:117] op_sel_hi:[0,1,1]
	v_pk_fma_f32 v[114:115], s[14:15], v[90:91], v[114:115] op_sel_hi:[0,1,1]
	v_pk_fma_f32 v[112:113], s[14:15], v[86:87], v[112:113] op_sel_hi:[0,1,1]
	s_cmp_lt_i32 s16, 4
	s_cbranch_scc0 .LBB0_1261

.LBB0_1270:
	s_waitcnt vmcnt(19)
	s_waitcnt lgkmcnt(0)
	v_readlane_b32 s14, v176, 4
	v_cvt_pk_f32_fp8_e32 v[80:81], v76
	v_cvt_pk_f32_fp8_sdwa v[82:83], v76 src0_sel:WORD_1
	v_cvt_pk_f32_fp8_e32 v[84:85], v77
	v_cvt_pk_f32_fp8_sdwa v[76:77], v77 src0_sel:WORD_1
	v_pk_fma_f32 v[126:127], v[80:81], s[14:15], v[126:127] op_sel_hi:[1,0,1]
	v_pk_fma_f32 v[124:125], v[82:83], s[14:15], v[124:125] op_sel_hi:[1,0,1]
	v_pk_fma_f32 v[120:121], s[14:15], v[76:77], v[120:121] op_sel_hi:[0,1,1]
	v_cvt_pk_f32_fp8_e32 v[76:77], v78
	v_cvt_pk_f32_fp8_sdwa v[80:81], v78 src0_sel:WORD_1
	v_cvt_pk_f32_fp8_e32 v[82:83], v79
	v_cvt_pk_f32_fp8_sdwa v[78:79], v79 src0_sel:WORD_1
	v_pk_fma_f32 v[122:123], s[14:15], v[84:85], v[122:123] op_sel_hi:[0,1,1]
	v_pk_fma_f32 v[118:119], s[14:15], v[76:77], v[118:119] op_sel_hi:[0,1,1]
	v_pk_fma_f32 v[116:117], s[14:15], v[80:81], v[116:117] op_sel_hi:[0,1,1]
	v_pk_fma_f32 v[114:115], s[14:15], v[82:83], v[114:115] op_sel_hi:[0,1,1]
	v_pk_fma_f32 v[112:113], s[14:15], v[78:79], v[112:113] op_sel_hi:[0,1,1]
	s_cmp_lt_i32 s16, 6
	s_cbranch_scc0 .LBB0_1263

.LBB0_1272:
	s_waitcnt vmcnt(17)
	s_waitcnt lgkmcnt(0)
	v_readlane_b32 s14, v176, 6
	v_cvt_pk_f32_fp8_e32 v[72:73], v68
	v_cvt_pk_f32_fp8_sdwa v[74:75], v68 src0_sel:WORD_1
	v_cvt_pk_f32_fp8_e32 v[76:77], v69
	v_cvt_pk_f32_fp8_sdwa v[68:69], v69 src0_sel:WORD_1
	v_pk_fma_f32 v[126:127], v[72:73], s[14:15], v[126:127] op_sel_hi:[1,0,1]
	v_pk_fma_f32 v[124:125], v[74:75], s[14:15], v[124:125] op_sel_hi:[1,0,1]
	v_pk_fma_f32 v[120:121], s[14:15], v[68:69], v[120:121] op_sel_hi:[0,1,1]
	v_cvt_pk_f32_fp8_e32 v[68:69], v70
	v_cvt_pk_f32_fp8_sdwa v[72:73], v70 src0_sel:WORD_1
	v_cvt_pk_f32_fp8_e32 v[74:75], v71
	v_cvt_pk_f32_fp8_sdwa v[70:71], v71 src0_sel:WORD_1
	v_pk_fma_f32 v[122:123], s[14:15], v[76:77], v[122:123] op_sel_hi:[0,1,1]
	v_pk_fma_f32 v[118:119], s[14:15], v[68:69], v[118:119] op_sel_hi:[0,1,1]
	v_pk_fma_f32 v[116:117], s[14:15], v[72:73], v[116:117] op_sel_hi:[0,1,1]
	v_pk_fma_f32 v[114:115], s[14:15], v[74:75], v[114:115] op_sel_hi:[0,1,1]
	v_pk_fma_f32 v[112:113], s[14:15], v[70:71], v[112:113] op_sel_hi:[0,1,1]
	s_cmp_lt_i32 s16, 8
	s_cbranch_scc0 .LBB0_1265

.LBB0_1276:
	s_waitcnt vmcnt(10)
	s_waitcnt lgkmcnt(0)
	v_readlane_b32 s14, v176, 2
	v_cvt_pk_f32_fp8_e32 v[178:179], v32
	v_cvt_pk_f32_fp8_sdwa v[180:181], v32 src0_sel:WORD_1
	v_cvt_pk_f32_fp8_e32 v[182:183], v33
	v_cvt_pk_f32_fp8_sdwa v[184:185], v33 src0_sel:WORD_1
	v_pk_fma_f32 v[210:211], v[178:179], s[14:15], v[210:211] op_sel_hi:[1,0,1]
	v_pk_fma_f32 v[212:213], v[180:181], s[14:15], v[212:213] op_sel_hi:[1,0,1]
	v_pk_fma_f32 v[214:215], s[14:15], v[182:183], v[214:215] op_sel_hi:[0,1,1]
	v_pk_fma_f32 v[216:217], s[14:15], v[184:185], v[216:217] op_sel_hi:[0,1,1]
	v_cvt_pk_f32_fp8_e32 v[178:179], v34
	v_cvt_pk_f32_fp8_sdwa v[180:181], v34 src0_sel:WORD_1
	v_cvt_pk_f32_fp8_e32 v[182:183], v35
	v_cvt_pk_f32_fp8_sdwa v[184:185], v35 src0_sel:WORD_1
	v_pk_fma_f32 v[218:219], s[14:15], v[178:179], v[218:219] op_sel_hi:[0,1,1]
	v_pk_fma_f32 v[220:221], s[14:15], v[180:181], v[220:221] op_sel_hi:[0,1,1]
	v_pk_fma_f32 v[222:223], s[14:15], v[182:183], v[222:223] op_sel_hi:[0,1,1]
	v_pk_fma_f32 v[224:225], s[14:15], v[184:185], v[224:225] op_sel_hi:[0,1,1]
	s_cmp_lt_i32 s16, 4
	s_cbranch_scc0 .LBB0_1132

.LBB0_1278:
	s_waitcnt vmcnt(19)
	s_waitcnt lgkmcnt(0)
	v_readlane_b32 s14, v176, 4
	v_cvt_pk_f32_fp8_e32 v[178:179], v16
	v_cvt_pk_f32_fp8_sdwa v[180:181], v16 src0_sel:WORD_1
	v_cvt_pk_f32_fp8_e32 v[182:183], v17
	v_cvt_pk_f32_fp8_sdwa v[184:185], v17 src0_sel:WORD_1
	v_pk_fma_f32 v[210:211], v[178:179], s[14:15], v[210:211] op_sel_hi:[1,0,1]
	v_pk_fma_f32 v[212:213], v[180:181], s[14:15], v[212:213] op_sel_hi:[1,0,1]
	v_pk_fma_f32 v[214:215], s[14:15], v[182:183], v[214:215] op_sel_hi:[0,1,1]
	v_pk_fma_f32 v[216:217], s[14:15], v[184:185], v[216:217] op_sel_hi:[0,1,1]
	s_waitcnt vmcnt(11)
	v_cvt_pk_f32_fp8_e32 v[178:179], v18
	v_cvt_pk_f32_fp8_sdwa v[180:181], v18 src0_sel:WORD_1
	v_cvt_pk_f32_fp8_e32 v[182:183], v19
	v_cvt_pk_f32_fp8_sdwa v[184:185], v19 src0_sel:WORD_1
	v_pk_fma_f32 v[218:219], s[14:15], v[178:179], v[218:219] op_sel_hi:[0,1,1]
	v_pk_fma_f32 v[220:221], s[14:15], v[180:181], v[220:221] op_sel_hi:[0,1,1]
	v_pk_fma_f32 v[222:223], s[14:15], v[182:183], v[222:223] op_sel_hi:[0,1,1]
	v_pk_fma_f32 v[224:225], s[14:15], v[184:185], v[224:225] op_sel_hi:[0,1,1]
	s_cmp_lt_i32 s16, 6
	s_cbranch_scc0 .LBB0_1134

.LBB0_1280:
	s_waitcnt vmcnt(17)
	s_waitcnt lgkmcnt(0)
	v_readlane_b32 s14, v176, 6
	v_cvt_pk_f32_fp8_e32 v[178:179], v4
	v_cvt_pk_f32_fp8_sdwa v[180:181], v4 src0_sel:WORD_1
	v_cvt_pk_f32_fp8_e32 v[182:183], v5
	v_cvt_pk_f32_fp8_sdwa v[184:185], v5 src0_sel:WORD_1
	v_pk_fma_f32 v[210:211], v[178:179], s[14:15], v[210:211] op_sel_hi:[1,0,1]
	v_pk_fma_f32 v[212:213], v[180:181], s[14:15], v[212:213] op_sel_hi:[1,0,1]
	v_pk_fma_f32 v[214:215], s[14:15], v[182:183], v[214:215] op_sel_hi:[0,1,1]
	v_pk_fma_f32 v[216:217], s[14:15], v[184:185], v[216:217] op_sel_hi:[0,1,1]
	v_cvt_pk_f32_fp8_e32 v[178:179], v6
	v_cvt_pk_f32_fp8_sdwa v[180:181], v6 src0_sel:WORD_1
	v_cvt_pk_f32_fp8_e32 v[182:183], v7
	v_cvt_pk_f32_fp8_sdwa v[184:185], v7 src0_sel:WORD_1
	v_pk_fma_f32 v[218:219], s[14:15], v[178:179], v[218:219] op_sel_hi:[0,1,1]
	v_pk_fma_f32 v[220:221], s[14:15], v[180:181], v[220:221] op_sel_hi:[0,1,1]
	v_pk_fma_f32 v[222:223], s[14:15], v[182:183], v[222:223] op_sel_hi:[0,1,1]
	v_pk_fma_f32 v[224:225], s[14:15], v[184:185], v[224:225] op_sel_hi:[0,1,1]
	s_cmp_lt_i32 s16, 8
	s_cbranch_scc0 .LBB0_1136
	s_branch .LBB0_1137

.LBB0_1282:
	s_waitcnt vmcnt(17)
	s_waitcnt lgkmcnt(0)
	v_readlane_b32 s14, v176, 2
	v_cvt_pk_f32_fp8_e32 v[178:179], v52
	v_cvt_pk_f32_fp8_sdwa v[180:181], v52 src0_sel:WORD_1
	v_cvt_pk_f32_fp8_e32 v[182:183], v53
	v_cvt_pk_f32_fp8_sdwa v[184:185], v53 src0_sel:WORD_1
	v_pk_fma_f32 v[210:211], v[178:179], s[14:15], v[210:211] op_sel_hi:[1,0,1]
	v_pk_fma_f32 v[212:213], v[180:181], s[14:15], v[212:213] op_sel_hi:[1,0,1]
	v_pk_fma_f32 v[214:215], s[14:15], v[182:183], v[214:215] op_sel_hi:[0,1,1]
	v_pk_fma_f32 v[216:217], s[14:15], v[184:185], v[216:217] op_sel_hi:[0,1,1]
	v_cvt_pk_f32_fp8_e32 v[178:179], v54
	v_cvt_pk_f32_fp8_sdwa v[180:181], v54 src0_sel:WORD_1
	v_cvt_pk_f32_fp8_e32 v[182:183], v55
	v_cvt_pk_f32_fp8_sdwa v[184:185], v55 src0_sel:WORD_1
	v_pk_fma_f32 v[218:219], s[14:15], v[178:179], v[218:219] op_sel_hi:[0,1,1]
	v_pk_fma_f32 v[220:221], s[14:15], v[180:181], v[220:221] op_sel_hi:[0,1,1]
	v_pk_fma_f32 v[222:223], s[14:15], v[182:183], v[222:223] op_sel_hi:[0,1,1]
	v_pk_fma_f32 v[224:225], s[14:15], v[184:185], v[224:225] op_sel_hi:[0,1,1]
	s_cmp_lt_i32 s16, 4
	s_cbranch_scc0 .LBB0_1190

.LBB0_1284:
	s_waitcnt vmcnt(19)
	s_waitcnt lgkmcnt(0)
	v_readlane_b32 s14, v176, 4
	v_cvt_pk_f32_fp8_e32 v[178:179], v40
	v_cvt_pk_f32_fp8_sdwa v[180:181], v40 src0_sel:WORD_1
	v_cvt_pk_f32_fp8_e32 v[182:183], v41
	v_cvt_pk_f32_fp8_sdwa v[184:185], v41 src0_sel:WORD_1
	v_pk_fma_f32 v[210:211], v[178:179], s[14:15], v[210:211] op_sel_hi:[1,0,1]
	v_pk_fma_f32 v[212:213], v[180:181], s[14:15], v[212:213] op_sel_hi:[1,0,1]
	v_pk_fma_f32 v[214:215], s[14:15], v[182:183], v[214:215] op_sel_hi:[0,1,1]
	v_pk_fma_f32 v[216:217], s[14:15], v[184:185], v[216:217] op_sel_hi:[0,1,1]
	v_cvt_pk_f32_fp8_e32 v[178:179], v42
	v_cvt_pk_f32_fp8_sdwa v[180:181], v42 src0_sel:WORD_1
	v_cvt_pk_f32_fp8_e32 v[182:183], v43
	v_cvt_pk_f32_fp8_sdwa v[184:185], v43 src0_sel:WORD_1
	v_pk_fma_f32 v[218:219], s[14:15], v[178:179], v[218:219] op_sel_hi:[0,1,1]
	v_pk_fma_f32 v[220:221], s[14:15], v[180:181], v[220:221] op_sel_hi:[0,1,1]
	v_pk_fma_f32 v[222:223], s[14:15], v[182:183], v[222:223] op_sel_hi:[0,1,1]
	v_pk_fma_f32 v[224:225], s[14:15], v[184:185], v[224:225] op_sel_hi:[0,1,1]
	s_cmp_lt_i32 s16, 6
	s_cbranch_scc0 .LBB0_1192

.LBB0_1286:
	s_waitcnt vmcnt(17)
	s_waitcnt lgkmcnt(0)
	v_readlane_b32 s14, v176, 6
	v_cvt_pk_f32_fp8_e32 v[178:179], v24
	v_cvt_pk_f32_fp8_sdwa v[180:181], v24 src0_sel:WORD_1
	v_cvt_pk_f32_fp8_e32 v[182:183], v25
	v_cvt_pk_f32_fp8_sdwa v[184:185], v25 src0_sel:WORD_1
	v_pk_fma_f32 v[210:211], v[178:179], s[14:15], v[210:211] op_sel_hi:[1,0,1]
	v_pk_fma_f32 v[212:213], v[180:181], s[14:15], v[212:213] op_sel_hi:[1,0,1]
	v_pk_fma_f32 v[214:215], s[14:15], v[182:183], v[214:215] op_sel_hi:[0,1,1]
	v_pk_fma_f32 v[216:217], s[14:15], v[184:185], v[216:217] op_sel_hi:[0,1,1]
	v_cvt_pk_f32_fp8_e32 v[178:179], v26
	v_cvt_pk_f32_fp8_sdwa v[180:181], v26 src0_sel:WORD_1
	v_cvt_pk_f32_fp8_e32 v[182:183], v27
	v_cvt_pk_f32_fp8_sdwa v[184:185], v27 src0_sel:WORD_1
	v_pk_fma_f32 v[218:219], s[14:15], v[178:179], v[218:219] op_sel_hi:[0,1,1]
	v_pk_fma_f32 v[220:221], s[14:15], v[180:181], v[220:221] op_sel_hi:[0,1,1]
	v_pk_fma_f32 v[222:223], s[14:15], v[182:183], v[222:223] op_sel_hi:[0,1,1]
	v_pk_fma_f32 v[224:225], s[14:15], v[184:185], v[224:225] op_sel_hi:[0,1,1]
	s_cmp_lt_i32 s16, 8
	s_cbranch_scc0 .LBB0_1194
	s_branch .LBB0_1195

.LBB0_1288:
	s_waitcnt vmcnt(21)
	s_waitcnt lgkmcnt(0)
	v_readlane_b32 s14, v176, 2
	v_cvt_pk_f32_fp8_e32 v[178:179], v84
	v_cvt_pk_f32_fp8_sdwa v[180:181], v84 src0_sel:WORD_1
	v_cvt_pk_f32_fp8_e32 v[182:183], v85
	v_cvt_pk_f32_fp8_sdwa v[184:185], v85 src0_sel:WORD_1
	v_pk_fma_f32 v[210:211], v[178:179], s[14:15], v[210:211] op_sel_hi:[1,0,1]
	v_pk_fma_f32 v[212:213], v[180:181], s[14:15], v[212:213] op_sel_hi:[1,0,1]
	v_pk_fma_f32 v[214:215], s[14:15], v[182:183], v[214:215] op_sel_hi:[0,1,1]
	v_pk_fma_f32 v[216:217], s[14:15], v[184:185], v[216:217] op_sel_hi:[0,1,1]
	v_cvt_pk_f32_fp8_e32 v[178:179], v86
	v_cvt_pk_f32_fp8_sdwa v[180:181], v86 src0_sel:WORD_1
	v_cvt_pk_f32_fp8_e32 v[182:183], v87
	v_cvt_pk_f32_fp8_sdwa v[184:185], v87 src0_sel:WORD_1
	v_pk_fma_f32 v[218:219], s[14:15], v[178:179], v[218:219] op_sel_hi:[0,1,1]
	v_pk_fma_f32 v[220:221], s[14:15], v[180:181], v[220:221] op_sel_hi:[0,1,1]
	v_pk_fma_f32 v[222:223], s[14:15], v[182:183], v[222:223] op_sel_hi:[0,1,1]
	v_pk_fma_f32 v[224:225], s[14:15], v[184:185], v[224:225] op_sel_hi:[0,1,1]
	s_cmp_lt_i32 s16, 4
	s_cbranch_scc0 .LBB0_1248

.LBB0_1290:
	s_waitcnt vmcnt(19)
	s_waitcnt lgkmcnt(0)
	v_readlane_b32 s14, v176, 4
	v_cvt_pk_f32_fp8_e32 v[178:179], v76
	v_cvt_pk_f32_fp8_sdwa v[180:181], v76 src0_sel:WORD_1
	v_cvt_pk_f32_fp8_e32 v[182:183], v77
	v_cvt_pk_f32_fp8_sdwa v[184:185], v77 src0_sel:WORD_1
	v_pk_fma_f32 v[210:211], v[178:179], s[14:15], v[210:211] op_sel_hi:[1,0,1]
	v_pk_fma_f32 v[212:213], v[180:181], s[14:15], v[212:213] op_sel_hi:[1,0,1]
	v_pk_fma_f32 v[214:215], s[14:15], v[182:183], v[214:215] op_sel_hi:[0,1,1]
	v_pk_fma_f32 v[216:217], s[14:15], v[184:185], v[216:217] op_sel_hi:[0,1,1]
	v_cvt_pk_f32_fp8_e32 v[178:179], v78
	v_cvt_pk_f32_fp8_sdwa v[180:181], v78 src0_sel:WORD_1
	v_cvt_pk_f32_fp8_e32 v[182:183], v79
	v_cvt_pk_f32_fp8_sdwa v[184:185], v79 src0_sel:WORD_1
	v_pk_fma_f32 v[218:219], s[14:15], v[178:179], v[218:219] op_sel_hi:[0,1,1]
	v_pk_fma_f32 v[220:221], s[14:15], v[180:181], v[220:221] op_sel_hi:[0,1,1]
	v_pk_fma_f32 v[222:223], s[14:15], v[182:183], v[222:223] op_sel_hi:[0,1,1]
	v_pk_fma_f32 v[224:225], s[14:15], v[184:185], v[224:225] op_sel_hi:[0,1,1]
	s_cmp_lt_i32 s16, 6
	s_cbranch_scc0 .LBB0_1250

.LBB0_1292:
	s_waitcnt vmcnt(17)
	s_waitcnt lgkmcnt(0)
	v_readlane_b32 s14, v176, 6
	v_cvt_pk_f32_fp8_e32 v[178:179], v68
	v_cvt_pk_f32_fp8_sdwa v[180:181], v68 src0_sel:WORD_1
	v_cvt_pk_f32_fp8_e32 v[182:183], v69
	v_cvt_pk_f32_fp8_sdwa v[184:185], v69 src0_sel:WORD_1
	v_pk_fma_f32 v[210:211], v[178:179], s[14:15], v[210:211] op_sel_hi:[1,0,1]
	v_pk_fma_f32 v[212:213], v[180:181], s[14:15], v[212:213] op_sel_hi:[1,0,1]
	v_pk_fma_f32 v[214:215], s[14:15], v[182:183], v[214:215] op_sel_hi:[0,1,1]
	v_pk_fma_f32 v[216:217], s[14:15], v[184:185], v[216:217] op_sel_hi:[0,1,1]
	v_cvt_pk_f32_fp8_e32 v[178:179], v70
	v_cvt_pk_f32_fp8_sdwa v[180:181], v70 src0_sel:WORD_1
	v_cvt_pk_f32_fp8_e32 v[182:183], v71
	v_cvt_pk_f32_fp8_sdwa v[184:185], v71 src0_sel:WORD_1
	v_pk_fma_f32 v[218:219], s[14:15], v[178:179], v[218:219] op_sel_hi:[0,1,1]
	v_pk_fma_f32 v[220:221], s[14:15], v[180:181], v[220:221] op_sel_hi:[0,1,1]
	v_pk_fma_f32 v[222:223], s[14:15], v[182:183], v[222:223] op_sel_hi:[0,1,1]
	v_pk_fma_f32 v[224:225], s[14:15], v[184:185], v[224:225] op_sel_hi:[0,1,1]
	s_cmp_lt_i32 s16, 8
	s_cbranch_scc0 .LBB0_1252
	s_branch .LBB0_1253

.LBB0_1294:
	s_waitcnt vmcnt(10)
	s_waitcnt lgkmcnt(0)
	v_readlane_b32 s14, v192, 2
	v_cvt_pk_f32_fp8_e32 v[194:195], v32
	v_cvt_pk_f32_fp8_sdwa v[196:197], v32 src0_sel:WORD_1
	v_cvt_pk_f32_fp8_e32 v[198:199], v33
	v_cvt_pk_f32_fp8_sdwa v[200:201], v33 src0_sel:WORD_1
	v_pk_fma_f32 v[188:189], v[194:195], s[14:15], v[188:189] op_sel_hi:[1,0,1]
	v_pk_fma_f32 v[184:185], v[196:197], s[14:15], v[184:185] op_sel_hi:[1,0,1]
	v_pk_fma_f32 v[180:181], s[14:15], v[198:199], v[180:181] op_sel_hi:[0,1,1]
	v_pk_fma_f32 v[176:177], s[14:15], v[200:201], v[176:177] op_sel_hi:[0,1,1]
	v_cvt_pk_f32_fp8_e32 v[194:195], v34
	v_cvt_pk_f32_fp8_sdwa v[196:197], v34 src0_sel:WORD_1
	v_cvt_pk_f32_fp8_e32 v[198:199], v35
	v_cvt_pk_f32_fp8_sdwa v[200:201], v35 src0_sel:WORD_1
	v_pk_fma_f32 v[190:191], s[14:15], v[194:195], v[190:191] op_sel_hi:[0,1,1]
	v_pk_fma_f32 v[186:187], s[14:15], v[196:197], v[186:187] op_sel_hi:[0,1,1]
	v_pk_fma_f32 v[182:183], s[14:15], v[198:199], v[182:183] op_sel_hi:[0,1,1]
	v_pk_fma_f32 v[178:179], s[14:15], v[200:201], v[178:179] op_sel_hi:[0,1,1]
	s_cmp_lt_i32 s16, 4
	s_cbranch_scc0 .LBB0_1107

.LBB0_1296:
	s_waitcnt vmcnt(19)
	s_waitcnt lgkmcnt(0)
	v_readlane_b32 s14, v192, 4
	v_cvt_pk_f32_fp8_e32 v[194:195], v16
	v_cvt_pk_f32_fp8_sdwa v[196:197], v16 src0_sel:WORD_1
	v_cvt_pk_f32_fp8_e32 v[198:199], v17
	v_cvt_pk_f32_fp8_sdwa v[200:201], v17 src0_sel:WORD_1
	v_pk_fma_f32 v[188:189], v[194:195], s[14:15], v[188:189] op_sel_hi:[1,0,1]
	v_pk_fma_f32 v[184:185], v[196:197], s[14:15], v[184:185] op_sel_hi:[1,0,1]
	v_pk_fma_f32 v[180:181], s[14:15], v[198:199], v[180:181] op_sel_hi:[0,1,1]
	v_pk_fma_f32 v[176:177], s[14:15], v[200:201], v[176:177] op_sel_hi:[0,1,1]
	s_waitcnt vmcnt(11)
	v_cvt_pk_f32_fp8_e32 v[194:195], v18
	v_cvt_pk_f32_fp8_sdwa v[196:197], v18 src0_sel:WORD_1
	v_cvt_pk_f32_fp8_e32 v[198:199], v19
	v_cvt_pk_f32_fp8_sdwa v[200:201], v19 src0_sel:WORD_1
	v_pk_fma_f32 v[190:191], s[14:15], v[194:195], v[190:191] op_sel_hi:[0,1,1]
	v_pk_fma_f32 v[186:187], s[14:15], v[196:197], v[186:187] op_sel_hi:[0,1,1]
	v_pk_fma_f32 v[182:183], s[14:15], v[198:199], v[182:183] op_sel_hi:[0,1,1]
	v_pk_fma_f32 v[178:179], s[14:15], v[200:201], v[178:179] op_sel_hi:[0,1,1]
	s_cmp_lt_i32 s16, 6
	s_cbranch_scc0 .LBB0_1109

.LBB0_1298:
	s_waitcnt vmcnt(17)
	s_waitcnt lgkmcnt(0)
	v_readlane_b32 s14, v192, 6
	v_cvt_pk_f32_fp8_e32 v[194:195], v4
	v_cvt_pk_f32_fp8_sdwa v[196:197], v4 src0_sel:WORD_1
	v_cvt_pk_f32_fp8_e32 v[198:199], v5
	v_cvt_pk_f32_fp8_sdwa v[200:201], v5 src0_sel:WORD_1
	v_pk_fma_f32 v[188:189], v[194:195], s[14:15], v[188:189] op_sel_hi:[1,0,1]
	v_pk_fma_f32 v[184:185], v[196:197], s[14:15], v[184:185] op_sel_hi:[1,0,1]
	v_pk_fma_f32 v[180:181], s[14:15], v[198:199], v[180:181] op_sel_hi:[0,1,1]
	v_pk_fma_f32 v[176:177], s[14:15], v[200:201], v[176:177] op_sel_hi:[0,1,1]
	v_cvt_pk_f32_fp8_e32 v[194:195], v6
	v_cvt_pk_f32_fp8_sdwa v[196:197], v6 src0_sel:WORD_1
	v_cvt_pk_f32_fp8_e32 v[198:199], v7
	v_cvt_pk_f32_fp8_sdwa v[200:201], v7 src0_sel:WORD_1
	v_pk_fma_f32 v[190:191], s[14:15], v[194:195], v[190:191] op_sel_hi:[0,1,1]
	v_pk_fma_f32 v[186:187], s[14:15], v[196:197], v[186:187] op_sel_hi:[0,1,1]
	v_pk_fma_f32 v[182:183], s[14:15], v[198:199], v[182:183] op_sel_hi:[0,1,1]
	v_pk_fma_f32 v[178:179], s[14:15], v[200:201], v[178:179] op_sel_hi:[0,1,1]
	s_cmp_lt_i32 s16, 8
	s_cbranch_scc0 .LBB0_1111
	s_branch .LBB0_1112

.LBB0_1300:
	s_waitcnt vmcnt(10)
	s_waitcnt lgkmcnt(0)
	v_readlane_b32 s14, v176, 2
	v_cvt_pk_f32_fp8_e32 v[178:179], v32
	v_cvt_pk_f32_fp8_sdwa v[180:181], v32 src0_sel:WORD_1
	v_cvt_pk_f32_fp8_e32 v[182:183], v33
	v_cvt_pk_f32_fp8_sdwa v[184:185], v33 src0_sel:WORD_1
	v_pk_fma_f32 v[198:199], v[178:179], s[14:15], v[198:199] op_sel_hi:[1,0,1]
	v_pk_fma_f32 v[196:197], v[180:181], s[14:15], v[196:197] op_sel_hi:[1,0,1]
	v_pk_fma_f32 v[194:195], s[14:15], v[182:183], v[194:195] op_sel_hi:[0,1,1]
	v_pk_fma_f32 v[192:193], s[14:15], v[184:185], v[192:193] op_sel_hi:[0,1,1]
	v_cvt_pk_f32_fp8_e32 v[178:179], v34
	v_cvt_pk_f32_fp8_sdwa v[180:181], v34 src0_sel:WORD_1
	v_cvt_pk_f32_fp8_e32 v[182:183], v35
	v_cvt_pk_f32_fp8_sdwa v[184:185], v35 src0_sel:WORD_1
	v_pk_fma_f32 v[208:209], s[14:15], v[178:179], v[208:209] op_sel_hi:[0,1,1]
	v_pk_fma_f32 v[206:207], s[14:15], v[180:181], v[206:207] op_sel_hi:[0,1,1]
	v_pk_fma_f32 v[204:205], s[14:15], v[182:183], v[204:205] op_sel_hi:[0,1,1]
	v_pk_fma_f32 v[200:201], s[14:15], v[184:185], v[200:201] op_sel_hi:[0,1,1]
	s_cmp_lt_i32 s16, 4
	s_cbranch_scc0 .LBB0_1119

.LBB0_1302:
	s_waitcnt vmcnt(19)
	s_waitcnt lgkmcnt(0)
	v_readlane_b32 s14, v176, 4
	v_cvt_pk_f32_fp8_e32 v[178:179], v16
	v_cvt_pk_f32_fp8_sdwa v[180:181], v16 src0_sel:WORD_1
	v_cvt_pk_f32_fp8_e32 v[182:183], v17
	v_cvt_pk_f32_fp8_sdwa v[184:185], v17 src0_sel:WORD_1
	v_pk_fma_f32 v[198:199], v[178:179], s[14:15], v[198:199] op_sel_hi:[1,0,1]
	v_pk_fma_f32 v[196:197], v[180:181], s[14:15], v[196:197] op_sel_hi:[1,0,1]
	v_pk_fma_f32 v[194:195], s[14:15], v[182:183], v[194:195] op_sel_hi:[0,1,1]
	v_pk_fma_f32 v[192:193], s[14:15], v[184:185], v[192:193] op_sel_hi:[0,1,1]
	s_waitcnt vmcnt(11)
	v_cvt_pk_f32_fp8_e32 v[178:179], v18
	v_cvt_pk_f32_fp8_sdwa v[180:181], v18 src0_sel:WORD_1
	v_cvt_pk_f32_fp8_e32 v[182:183], v19
	v_cvt_pk_f32_fp8_sdwa v[184:185], v19 src0_sel:WORD_1
	v_pk_fma_f32 v[208:209], s[14:15], v[178:179], v[208:209] op_sel_hi:[0,1,1]
	v_pk_fma_f32 v[206:207], s[14:15], v[180:181], v[206:207] op_sel_hi:[0,1,1]
	v_pk_fma_f32 v[204:205], s[14:15], v[182:183], v[204:205] op_sel_hi:[0,1,1]
	v_pk_fma_f32 v[200:201], s[14:15], v[184:185], v[200:201] op_sel_hi:[0,1,1]
	s_cmp_lt_i32 s16, 6
	s_cbranch_scc0 .LBB0_1121

.LBB0_1304:
	s_waitcnt vmcnt(17)
	s_waitcnt lgkmcnt(0)
	v_readlane_b32 s14, v176, 6
	v_cvt_pk_f32_fp8_e32 v[178:179], v4
	v_cvt_pk_f32_fp8_sdwa v[180:181], v4 src0_sel:WORD_1
	v_cvt_pk_f32_fp8_e32 v[182:183], v5
	v_cvt_pk_f32_fp8_sdwa v[184:185], v5 src0_sel:WORD_1
	v_pk_fma_f32 v[198:199], v[178:179], s[14:15], v[198:199] op_sel_hi:[1,0,1]
	v_pk_fma_f32 v[196:197], v[180:181], s[14:15], v[196:197] op_sel_hi:[1,0,1]
	v_pk_fma_f32 v[194:195], s[14:15], v[182:183], v[194:195] op_sel_hi:[0,1,1]
	v_pk_fma_f32 v[192:193], s[14:15], v[184:185], v[192:193] op_sel_hi:[0,1,1]
	v_cvt_pk_f32_fp8_e32 v[178:179], v6
	v_cvt_pk_f32_fp8_sdwa v[180:181], v6 src0_sel:WORD_1
	v_cvt_pk_f32_fp8_e32 v[182:183], v7
	v_cvt_pk_f32_fp8_sdwa v[184:185], v7 src0_sel:WORD_1
	v_pk_fma_f32 v[208:209], s[14:15], v[178:179], v[208:209] op_sel_hi:[0,1,1]
	v_pk_fma_f32 v[206:207], s[14:15], v[180:181], v[206:207] op_sel_hi:[0,1,1]
	v_pk_fma_f32 v[204:205], s[14:15], v[182:183], v[204:205] op_sel_hi:[0,1,1]
	v_pk_fma_f32 v[200:201], s[14:15], v[184:185], v[200:201] op_sel_hi:[0,1,1]
	s_cmp_lt_i32 s16, 8
	s_cbranch_scc0 .LBB0_1123
	s_branch .LBB0_1124

.LBB0_1306:
	s_waitcnt vmcnt(17)
	s_waitcnt lgkmcnt(0)
	v_readlane_b32 s14, v192, 2
	v_cvt_pk_f32_fp8_e32 v[194:195], v52
	v_cvt_pk_f32_fp8_sdwa v[196:197], v52 src0_sel:WORD_1
	v_cvt_pk_f32_fp8_e32 v[198:199], v53
	v_cvt_pk_f32_fp8_sdwa v[200:201], v53 src0_sel:WORD_1
	v_pk_fma_f32 v[188:189], v[194:195], s[14:15], v[188:189] op_sel_hi:[1,0,1]
	v_pk_fma_f32 v[184:185], v[196:197], s[14:15], v[184:185] op_sel_hi:[1,0,1]
	v_pk_fma_f32 v[180:181], s[14:15], v[198:199], v[180:181] op_sel_hi:[0,1,1]
	v_pk_fma_f32 v[176:177], s[14:15], v[200:201], v[176:177] op_sel_hi:[0,1,1]
	v_cvt_pk_f32_fp8_e32 v[194:195], v54
	v_cvt_pk_f32_fp8_sdwa v[196:197], v54 src0_sel:WORD_1
	v_cvt_pk_f32_fp8_e32 v[198:199], v55
	v_cvt_pk_f32_fp8_sdwa v[200:201], v55 src0_sel:WORD_1
	v_pk_fma_f32 v[190:191], s[14:15], v[194:195], v[190:191] op_sel_hi:[0,1,1]
	v_pk_fma_f32 v[186:187], s[14:15], v[196:197], v[186:187] op_sel_hi:[0,1,1]
	v_pk_fma_f32 v[182:183], s[14:15], v[198:199], v[182:183] op_sel_hi:[0,1,1]
	v_pk_fma_f32 v[178:179], s[14:15], v[200:201], v[178:179] op_sel_hi:[0,1,1]
	s_cmp_lt_i32 s16, 4
	s_cbranch_scc0 .LBB0_1165

.LBB0_1308:
	s_waitcnt vmcnt(19)
	s_waitcnt lgkmcnt(0)
	v_readlane_b32 s14, v192, 4
	v_cvt_pk_f32_fp8_e32 v[194:195], v40
	v_cvt_pk_f32_fp8_sdwa v[196:197], v40 src0_sel:WORD_1
	v_cvt_pk_f32_fp8_e32 v[198:199], v41
	v_cvt_pk_f32_fp8_sdwa v[200:201], v41 src0_sel:WORD_1
	v_pk_fma_f32 v[188:189], v[194:195], s[14:15], v[188:189] op_sel_hi:[1,0,1]
	v_pk_fma_f32 v[184:185], v[196:197], s[14:15], v[184:185] op_sel_hi:[1,0,1]
	v_pk_fma_f32 v[180:181], s[14:15], v[198:199], v[180:181] op_sel_hi:[0,1,1]
	v_pk_fma_f32 v[176:177], s[14:15], v[200:201], v[176:177] op_sel_hi:[0,1,1]
	v_cvt_pk_f32_fp8_e32 v[194:195], v42
	v_cvt_pk_f32_fp8_sdwa v[196:197], v42 src0_sel:WORD_1
	v_cvt_pk_f32_fp8_e32 v[198:199], v43
	v_cvt_pk_f32_fp8_sdwa v[200:201], v43 src0_sel:WORD_1
	v_pk_fma_f32 v[190:191], s[14:15], v[194:195], v[190:191] op_sel_hi:[0,1,1]
	v_pk_fma_f32 v[186:187], s[14:15], v[196:197], v[186:187] op_sel_hi:[0,1,1]
	v_pk_fma_f32 v[182:183], s[14:15], v[198:199], v[182:183] op_sel_hi:[0,1,1]
	v_pk_fma_f32 v[178:179], s[14:15], v[200:201], v[178:179] op_sel_hi:[0,1,1]
	s_cmp_lt_i32 s16, 6
	s_cbranch_scc0 .LBB0_1167

.LBB0_1310:
	s_waitcnt vmcnt(17)
	s_waitcnt lgkmcnt(0)
	v_readlane_b32 s14, v192, 6
	v_cvt_pk_f32_fp8_e32 v[194:195], v24
	v_cvt_pk_f32_fp8_sdwa v[196:197], v24 src0_sel:WORD_1
	v_cvt_pk_f32_fp8_e32 v[198:199], v25
	v_cvt_pk_f32_fp8_sdwa v[200:201], v25 src0_sel:WORD_1
	v_pk_fma_f32 v[188:189], v[194:195], s[14:15], v[188:189] op_sel_hi:[1,0,1]
	v_pk_fma_f32 v[184:185], v[196:197], s[14:15], v[184:185] op_sel_hi:[1,0,1]
	v_pk_fma_f32 v[180:181], s[14:15], v[198:199], v[180:181] op_sel_hi:[0,1,1]
	v_pk_fma_f32 v[176:177], s[14:15], v[200:201], v[176:177] op_sel_hi:[0,1,1]
	v_cvt_pk_f32_fp8_e32 v[194:195], v26
	v_cvt_pk_f32_fp8_sdwa v[196:197], v26 src0_sel:WORD_1
	v_cvt_pk_f32_fp8_e32 v[198:199], v27
	v_cvt_pk_f32_fp8_sdwa v[200:201], v27 src0_sel:WORD_1
	v_pk_fma_f32 v[190:191], s[14:15], v[194:195], v[190:191] op_sel_hi:[0,1,1]
	v_pk_fma_f32 v[186:187], s[14:15], v[196:197], v[186:187] op_sel_hi:[0,1,1]
	v_pk_fma_f32 v[182:183], s[14:15], v[198:199], v[182:183] op_sel_hi:[0,1,1]
	v_pk_fma_f32 v[178:179], s[14:15], v[200:201], v[178:179] op_sel_hi:[0,1,1]
	s_cmp_lt_i32 s16, 8
	s_cbranch_scc0 .LBB0_1169
	s_branch .LBB0_1170

.LBB0_1312:
	s_waitcnt vmcnt(17)
	s_waitcnt lgkmcnt(0)
	v_readlane_b32 s14, v176, 2
	v_cvt_pk_f32_fp8_e32 v[178:179], v52
	v_cvt_pk_f32_fp8_sdwa v[180:181], v52 src0_sel:WORD_1
	v_cvt_pk_f32_fp8_e32 v[182:183], v53
	v_cvt_pk_f32_fp8_sdwa v[184:185], v53 src0_sel:WORD_1
	v_pk_fma_f32 v[198:199], v[178:179], s[14:15], v[198:199] op_sel_hi:[1,0,1]
	v_pk_fma_f32 v[196:197], v[180:181], s[14:15], v[196:197] op_sel_hi:[1,0,1]
	v_pk_fma_f32 v[194:195], s[14:15], v[182:183], v[194:195] op_sel_hi:[0,1,1]
	v_pk_fma_f32 v[192:193], s[14:15], v[184:185], v[192:193] op_sel_hi:[0,1,1]
	v_cvt_pk_f32_fp8_e32 v[178:179], v54
	v_cvt_pk_f32_fp8_sdwa v[180:181], v54 src0_sel:WORD_1
	v_cvt_pk_f32_fp8_e32 v[182:183], v55
	v_cvt_pk_f32_fp8_sdwa v[184:185], v55 src0_sel:WORD_1
	v_pk_fma_f32 v[208:209], s[14:15], v[178:179], v[208:209] op_sel_hi:[0,1,1]
	v_pk_fma_f32 v[206:207], s[14:15], v[180:181], v[206:207] op_sel_hi:[0,1,1]
	v_pk_fma_f32 v[204:205], s[14:15], v[182:183], v[204:205] op_sel_hi:[0,1,1]
	v_pk_fma_f32 v[200:201], s[14:15], v[184:185], v[200:201] op_sel_hi:[0,1,1]
	s_cmp_lt_i32 s16, 4
	s_cbranch_scc0 .LBB0_1177

.LBB0_1314:
	s_waitcnt vmcnt(19)
	s_waitcnt lgkmcnt(0)
	v_readlane_b32 s14, v176, 4
	v_cvt_pk_f32_fp8_e32 v[178:179], v40
	v_cvt_pk_f32_fp8_sdwa v[180:181], v40 src0_sel:WORD_1
	v_cvt_pk_f32_fp8_e32 v[182:183], v41
	v_cvt_pk_f32_fp8_sdwa v[184:185], v41 src0_sel:WORD_1
	v_pk_fma_f32 v[198:199], v[178:179], s[14:15], v[198:199] op_sel_hi:[1,0,1]
	v_pk_fma_f32 v[196:197], v[180:181], s[14:15], v[196:197] op_sel_hi:[1,0,1]
	v_pk_fma_f32 v[194:195], s[14:15], v[182:183], v[194:195] op_sel_hi:[0,1,1]
	v_pk_fma_f32 v[192:193], s[14:15], v[184:185], v[192:193] op_sel_hi:[0,1,1]
	v_cvt_pk_f32_fp8_e32 v[178:179], v42
	v_cvt_pk_f32_fp8_sdwa v[180:181], v42 src0_sel:WORD_1
	v_cvt_pk_f32_fp8_e32 v[182:183], v43
	v_cvt_pk_f32_fp8_sdwa v[184:185], v43 src0_sel:WORD_1
	v_pk_fma_f32 v[208:209], s[14:15], v[178:179], v[208:209] op_sel_hi:[0,1,1]
	v_pk_fma_f32 v[206:207], s[14:15], v[180:181], v[206:207] op_sel_hi:[0,1,1]
	v_pk_fma_f32 v[204:205], s[14:15], v[182:183], v[204:205] op_sel_hi:[0,1,1]
	v_pk_fma_f32 v[200:201], s[14:15], v[184:185], v[200:201] op_sel_hi:[0,1,1]
	s_cmp_lt_i32 s16, 6
	s_cbranch_scc0 .LBB0_1179

.LBB0_1316:
	s_waitcnt vmcnt(17)
	s_waitcnt lgkmcnt(0)
	v_readlane_b32 s14, v176, 6
	v_cvt_pk_f32_fp8_e32 v[178:179], v24
	v_cvt_pk_f32_fp8_sdwa v[180:181], v24 src0_sel:WORD_1
	v_cvt_pk_f32_fp8_e32 v[182:183], v25
	v_cvt_pk_f32_fp8_sdwa v[184:185], v25 src0_sel:WORD_1
	v_pk_fma_f32 v[198:199], v[178:179], s[14:15], v[198:199] op_sel_hi:[1,0,1]
	v_pk_fma_f32 v[196:197], v[180:181], s[14:15], v[196:197] op_sel_hi:[1,0,1]
	v_pk_fma_f32 v[194:195], s[14:15], v[182:183], v[194:195] op_sel_hi:[0,1,1]
	v_pk_fma_f32 v[192:193], s[14:15], v[184:185], v[192:193] op_sel_hi:[0,1,1]
	v_cvt_pk_f32_fp8_e32 v[178:179], v26
	v_cvt_pk_f32_fp8_sdwa v[180:181], v26 src0_sel:WORD_1
	v_cvt_pk_f32_fp8_e32 v[182:183], v27
	v_cvt_pk_f32_fp8_sdwa v[184:185], v27 src0_sel:WORD_1
	v_pk_fma_f32 v[208:209], s[14:15], v[178:179], v[208:209] op_sel_hi:[0,1,1]
	v_pk_fma_f32 v[206:207], s[14:15], v[180:181], v[206:207] op_sel_hi:[0,1,1]
	v_pk_fma_f32 v[204:205], s[14:15], v[182:183], v[204:205] op_sel_hi:[0,1,1]
	v_pk_fma_f32 v[200:201], s[14:15], v[184:185], v[200:201] op_sel_hi:[0,1,1]
	s_cmp_lt_i32 s16, 8
	s_cbranch_scc0 .LBB0_1181
	s_branch .LBB0_1182

.LBB0_1318:
	s_waitcnt vmcnt(21)
	s_waitcnt lgkmcnt(0)
	v_readlane_b32 s14, v192, 2
	v_cvt_pk_f32_fp8_e32 v[194:195], v84
	v_cvt_pk_f32_fp8_sdwa v[196:197], v84 src0_sel:WORD_1
	v_cvt_pk_f32_fp8_e32 v[198:199], v85
	v_cvt_pk_f32_fp8_sdwa v[200:201], v85 src0_sel:WORD_1
	v_pk_fma_f32 v[188:189], v[194:195], s[14:15], v[188:189] op_sel_hi:[1,0,1]
	v_pk_fma_f32 v[184:185], v[196:197], s[14:15], v[184:185] op_sel_hi:[1,0,1]
	v_pk_fma_f32 v[180:181], s[14:15], v[198:199], v[180:181] op_sel_hi:[0,1,1]
	v_pk_fma_f32 v[176:177], s[14:15], v[200:201], v[176:177] op_sel_hi:[0,1,1]
	v_cvt_pk_f32_fp8_e32 v[194:195], v86
	v_cvt_pk_f32_fp8_sdwa v[196:197], v86 src0_sel:WORD_1
	v_cvt_pk_f32_fp8_e32 v[198:199], v87
	v_cvt_pk_f32_fp8_sdwa v[200:201], v87 src0_sel:WORD_1
	v_pk_fma_f32 v[190:191], s[14:15], v[194:195], v[190:191] op_sel_hi:[0,1,1]
	v_pk_fma_f32 v[186:187], s[14:15], v[196:197], v[186:187] op_sel_hi:[0,1,1]
	v_pk_fma_f32 v[182:183], s[14:15], v[198:199], v[182:183] op_sel_hi:[0,1,1]
	v_pk_fma_f32 v[178:179], s[14:15], v[200:201], v[178:179] op_sel_hi:[0,1,1]
	s_cmp_lt_i32 s16, 4
	s_cbranch_scc0 .LBB0_1223

.LBB0_1320:
	s_waitcnt vmcnt(19)
	s_waitcnt lgkmcnt(0)
	v_readlane_b32 s14, v192, 4
	v_cvt_pk_f32_fp8_e32 v[194:195], v76
	v_cvt_pk_f32_fp8_sdwa v[196:197], v76 src0_sel:WORD_1
	v_cvt_pk_f32_fp8_e32 v[198:199], v77
	v_cvt_pk_f32_fp8_sdwa v[200:201], v77 src0_sel:WORD_1
	v_pk_fma_f32 v[188:189], v[194:195], s[14:15], v[188:189] op_sel_hi:[1,0,1]
	v_pk_fma_f32 v[184:185], v[196:197], s[14:15], v[184:185] op_sel_hi:[1,0,1]
	v_pk_fma_f32 v[180:181], s[14:15], v[198:199], v[180:181] op_sel_hi:[0,1,1]
	v_pk_fma_f32 v[176:177], s[14:15], v[200:201], v[176:177] op_sel_hi:[0,1,1]
	v_cvt_pk_f32_fp8_e32 v[194:195], v78
	v_cvt_pk_f32_fp8_sdwa v[196:197], v78 src0_sel:WORD_1
	v_cvt_pk_f32_fp8_e32 v[198:199], v79
	v_cvt_pk_f32_fp8_sdwa v[200:201], v79 src0_sel:WORD_1
	v_pk_fma_f32 v[190:191], s[14:15], v[194:195], v[190:191] op_sel_hi:[0,1,1]
	v_pk_fma_f32 v[186:187], s[14:15], v[196:197], v[186:187] op_sel_hi:[0,1,1]
	v_pk_fma_f32 v[182:183], s[14:15], v[198:199], v[182:183] op_sel_hi:[0,1,1]
	v_pk_fma_f32 v[178:179], s[14:15], v[200:201], v[178:179] op_sel_hi:[0,1,1]
	s_cmp_lt_i32 s16, 6
	s_cbranch_scc0 .LBB0_1225

.LBB0_1322:
	s_waitcnt vmcnt(17)
	s_waitcnt lgkmcnt(0)
	v_readlane_b32 s14, v192, 6
	v_cvt_pk_f32_fp8_e32 v[194:195], v68
	v_cvt_pk_f32_fp8_sdwa v[196:197], v68 src0_sel:WORD_1
	v_cvt_pk_f32_fp8_e32 v[198:199], v69
	v_cvt_pk_f32_fp8_sdwa v[200:201], v69 src0_sel:WORD_1
	v_pk_fma_f32 v[188:189], v[194:195], s[14:15], v[188:189] op_sel_hi:[1,0,1]
	v_pk_fma_f32 v[184:185], v[196:197], s[14:15], v[184:185] op_sel_hi:[1,0,1]
	v_pk_fma_f32 v[180:181], s[14:15], v[198:199], v[180:181] op_sel_hi:[0,1,1]
	v_pk_fma_f32 v[176:177], s[14:15], v[200:201], v[176:177] op_sel_hi:[0,1,1]
	v_cvt_pk_f32_fp8_e32 v[194:195], v70
	v_cvt_pk_f32_fp8_sdwa v[196:197], v70 src0_sel:WORD_1
	v_cvt_pk_f32_fp8_e32 v[198:199], v71
	v_cvt_pk_f32_fp8_sdwa v[200:201], v71 src0_sel:WORD_1
	v_pk_fma_f32 v[190:191], s[14:15], v[194:195], v[190:191] op_sel_hi:[0,1,1]
	v_pk_fma_f32 v[186:187], s[14:15], v[196:197], v[186:187] op_sel_hi:[0,1,1]
	v_pk_fma_f32 v[182:183], s[14:15], v[198:199], v[182:183] op_sel_hi:[0,1,1]
	v_pk_fma_f32 v[178:179], s[14:15], v[200:201], v[178:179] op_sel_hi:[0,1,1]
	s_cmp_lt_i32 s16, 8
	s_cbranch_scc0 .LBB0_1227
	s_branch .LBB0_1228

.LBB0_1324:
	s_waitcnt vmcnt(21)
	s_waitcnt lgkmcnt(0)
	v_readlane_b32 s14, v176, 2
	v_cvt_pk_f32_fp8_e32 v[178:179], v84
	v_cvt_pk_f32_fp8_sdwa v[180:181], v84 src0_sel:WORD_1
	v_cvt_pk_f32_fp8_e32 v[182:183], v85
	v_cvt_pk_f32_fp8_sdwa v[184:185], v85 src0_sel:WORD_1
	v_pk_fma_f32 v[198:199], v[178:179], s[14:15], v[198:199] op_sel_hi:[1,0,1]
	v_pk_fma_f32 v[196:197], v[180:181], s[14:15], v[196:197] op_sel_hi:[1,0,1]
	v_pk_fma_f32 v[194:195], s[14:15], v[182:183], v[194:195] op_sel_hi:[0,1,1]
	v_pk_fma_f32 v[192:193], s[14:15], v[184:185], v[192:193] op_sel_hi:[0,1,1]
	v_cvt_pk_f32_fp8_e32 v[178:179], v86
	v_cvt_pk_f32_fp8_sdwa v[180:181], v86 src0_sel:WORD_1
	v_cvt_pk_f32_fp8_e32 v[182:183], v87
	v_cvt_pk_f32_fp8_sdwa v[184:185], v87 src0_sel:WORD_1
	v_pk_fma_f32 v[208:209], s[14:15], v[178:179], v[208:209] op_sel_hi:[0,1,1]
	v_pk_fma_f32 v[206:207], s[14:15], v[180:181], v[206:207] op_sel_hi:[0,1,1]
	v_pk_fma_f32 v[204:205], s[14:15], v[182:183], v[204:205] op_sel_hi:[0,1,1]
	v_pk_fma_f32 v[200:201], s[14:15], v[184:185], v[200:201] op_sel_hi:[0,1,1]
	s_cmp_lt_i32 s16, 4
	s_cbranch_scc0 .LBB0_1235

.LBB0_1326:
	s_waitcnt vmcnt(19)
	s_waitcnt lgkmcnt(0)
	v_readlane_b32 s14, v176, 4
	v_cvt_pk_f32_fp8_e32 v[178:179], v76
	v_cvt_pk_f32_fp8_sdwa v[180:181], v76 src0_sel:WORD_1
	v_cvt_pk_f32_fp8_e32 v[182:183], v77
	v_cvt_pk_f32_fp8_sdwa v[184:185], v77 src0_sel:WORD_1
	v_pk_fma_f32 v[198:199], v[178:179], s[14:15], v[198:199] op_sel_hi:[1,0,1]
	v_pk_fma_f32 v[196:197], v[180:181], s[14:15], v[196:197] op_sel_hi:[1,0,1]
	v_pk_fma_f32 v[194:195], s[14:15], v[182:183], v[194:195] op_sel_hi:[0,1,1]
	v_pk_fma_f32 v[192:193], s[14:15], v[184:185], v[192:193] op_sel_hi:[0,1,1]
	v_cvt_pk_f32_fp8_e32 v[178:179], v78
	v_cvt_pk_f32_fp8_sdwa v[180:181], v78 src0_sel:WORD_1
	v_cvt_pk_f32_fp8_e32 v[182:183], v79
	v_cvt_pk_f32_fp8_sdwa v[184:185], v79 src0_sel:WORD_1
	v_pk_fma_f32 v[208:209], s[14:15], v[178:179], v[208:209] op_sel_hi:[0,1,1]
	v_pk_fma_f32 v[206:207], s[14:15], v[180:181], v[206:207] op_sel_hi:[0,1,1]
	v_pk_fma_f32 v[204:205], s[14:15], v[182:183], v[204:205] op_sel_hi:[0,1,1]
	v_pk_fma_f32 v[200:201], s[14:15], v[184:185], v[200:201] op_sel_hi:[0,1,1]
	s_cmp_lt_i32 s16, 6
	s_cbranch_scc0 .LBB0_1237

.LBB0_1328:
	s_waitcnt vmcnt(17)
	s_waitcnt lgkmcnt(0)
	v_readlane_b32 s14, v176, 6
	v_cvt_pk_f32_fp8_e32 v[178:179], v68
	v_cvt_pk_f32_fp8_sdwa v[180:181], v68 src0_sel:WORD_1
	v_cvt_pk_f32_fp8_e32 v[182:183], v69
	v_cvt_pk_f32_fp8_sdwa v[184:185], v69 src0_sel:WORD_1
	v_pk_fma_f32 v[198:199], v[178:179], s[14:15], v[198:199] op_sel_hi:[1,0,1]
	v_pk_fma_f32 v[196:197], v[180:181], s[14:15], v[196:197] op_sel_hi:[1,0,1]
	v_pk_fma_f32 v[194:195], s[14:15], v[182:183], v[194:195] op_sel_hi:[0,1,1]
	v_pk_fma_f32 v[192:193], s[14:15], v[184:185], v[192:193] op_sel_hi:[0,1,1]
	v_cvt_pk_f32_fp8_e32 v[178:179], v70
	v_cvt_pk_f32_fp8_sdwa v[180:181], v70 src0_sel:WORD_1
	v_cvt_pk_f32_fp8_e32 v[182:183], v71
	v_cvt_pk_f32_fp8_sdwa v[184:185], v71 src0_sel:WORD_1
	v_pk_fma_f32 v[208:209], s[14:15], v[178:179], v[208:209] op_sel_hi:[0,1,1]
	v_pk_fma_f32 v[206:207], s[14:15], v[180:181], v[206:207] op_sel_hi:[0,1,1]
	v_pk_fma_f32 v[204:205], s[14:15], v[182:183], v[204:205] op_sel_hi:[0,1,1]
	v_pk_fma_f32 v[200:201], s[14:15], v[184:185], v[200:201] op_sel_hi:[0,1,1]
	s_cmp_lt_i32 s16, 8
	s_cbranch_scc0 .LBB0_1239
	s_branch .LBB0_1240
